# W_in token-major epilogue: per-row token scales pre-loaded once per unit so result stores are no longer drained before each row
# baseline (speedup 1.0000x reference)
; #define GAS __attribute__((address_space(1)))
; __device__ __forceinline__ v4u pack8(const f32x4 a, const f32x4 b) { v4u w; w.x = cvt_pk_bf16(a[0], a[1]); w.y = cvt_pk_bf16(a[2], a[3]); w.z = cvt_pk_bf16(b[0], b[1]); w.w = cvt_pk_bf16(b[2], b[3]); return w; }
; __device__ __forceinline__ float fexp(float x) { return __builtin_amdgcn_exp2f(x * 1.4426950408889634f); }
; #define EPI_LOOP_AM for (int ai = 0; ai < 2; ++ai) _Pragma("unroll") for (int m = 0; m < 4; ++m)
;     __device__ __forceinline__ void operator()(AccI& acci, const Unit& u, LAS unsigned char*, int wr, int wc, int fr, int fq) const {
;         const int pm = u.p0, pn = u.p1, c0 = wc * 32 + 8 * fq;
;         f32x4 swc[2][2];
; #pragma unroll
;         for (int bj = 0; bj < 2; ++bj)
; #pragma unroll
;             for (int n = 0; n < 2; ++n) swc[bj][n] = *(const GAS f32x4*)(swin + u.p2 + 128 * bj + c0 + 4 * n);
;     ...
; #pragma unroll
;             EPI_LOOP_AM {
;                 const int r = 128 * ai + 64 * wr + 16 * m + fr, tok = pm * 256 + r; const float sxr = sx0[tok];
; #pragma unroll
;                 for (int bj = 0; bj < 2; ++bj) { f32x4 v[2];
; #pragma unroll
;                     for (int n = 0; n < 2; ++n)
; #pragma unroll
;                         for (int j = 0; j < 4; ++j) { const float g = ACCF(ai, bj, m, n, j); v[n][j] = g * __builtin_amdgcn_rcpf(1.f + fexp(-g)); }
;                     *(GAS v4u*)(gs + (size_t)tok * RW + (pn - 8) * 256 + bj * 128 + c0) = pack8(v[0], v[1]); }
;             }
.LBB0_182:
	s_ashr_i32 s73, s72, 31
	v_mov_b32_e32 v154, v161
	s_waitcnt vmcnt(0)
	v_mov_b32_e32 v32, v162
	s_lshl_b64 s[72:73], s[72:73], 2
	s_add_u32 s72, s36, s72
	v_lshl_add_u32 v150, v32, 3, s27
	s_addc_u32 s73, s37, s73
	v_ashrrev_i32_e32 v151, 31, v150
	v_lshl_add_u64 v[44:45], v[150:151], 2, s[72:73]
	global_load_dwordx4 v[32:35], v[44:45], off offset:16
	global_load_dwordx4 v[40:43], v[44:45], off
	global_load_dwordx4 v[36:39], v[44:45], off offset:528
	s_nop 0
	global_load_dwordx4 v[44:47], v[44:45], off offset:512
	s_cmp_lt_i32 s24, 8
	s_mov_b64 s[72:73], -1
	s_cbranch_scc1 .LBB0_184
	s_lshl_b32 s0, s4, 8
	s_add_i32 s0, s0, s26
	v_add_u32_e32 v144, s0, v154
	v_ashrrev_i32_e32 v145, 31, v144
	v_lshl_add_u64 v[146:147], v[144:145], 2, s[34:35]
	global_load_dword v148, v[146:147], off
	global_load_dword v216, v[146:147], off offset:64
	global_load_dword v217, v[146:147], off offset:128
	global_load_dword v218, v[146:147], off offset:192
	global_load_dword v219, v[146:147], off offset:512
	global_load_dword v220, v[146:147], off offset:576
	global_load_dword v221, v[146:147], off offset:640
	global_load_dword v222, v[146:147], off offset:704
	v_lshlrev_b64 v[146:147], 11, v[144:145]
	v_cvt_f32_i32_e32 v145, v140
	s_lshl_b32 s0, s24, 8
	s_add_i32 s6, s0, 0xfffff800
	v_lshl_add_u64 v[146:147], s[42:43], 0, v[146:147]
	s_lshl_b64 s[72:73], s[6:7], 1
	s_waitcnt vmcnt(0)
	v_mul_f32_e32 v152, v40, v148
	v_mul_f32_e32 v145, v152, v145
	v_mul_f32_e32 v152, 0xbfb8aa3b, v145
	v_exp_f32_e32 v152, v152
	v_mul_f32_e32 v153, v41, v148
	v_mul_f32_e32 v155, v42, v148
	v_mul_f32_e32 v156, v43, v148
	v_add_f32_e32 v152, 1.0, v152
	v_rcp_f32_e32 v152, v152
	v_mul_f32_e32 v157, v32, v148
	v_mul_f32_e32 v145, v145, v152
	v_cvt_f32_i32_e32 v152, v141
	v_mul_f32_e32 v152, v153, v152
	v_mul_f32_e32 v153, 0xbfb8aa3b, v152
	v_exp_f32_e32 v153, v153
	s_nop 0
	v_add_f32_e32 v153, 1.0, v153
	v_rcp_f32_e32 v153, v153
	s_nop 0
	v_mul_f32_e32 v152, v152, v153
	v_cvt_f32_i32_e32 v153, v142
	v_mul_f32_e32 v153, v155, v153
	v_mul_f32_e32 v155, 0xbfb8aa3b, v153
	v_exp_f32_e32 v155, v155
	s_nop 0
	v_add_f32_e32 v155, 1.0, v155
	v_rcp_f32_e32 v155, v155
	s_nop 0
	v_mul_f32_e32 v153, v153, v155
	v_cvt_f32_i32_e32 v155, v143
	v_mul_f32_e32 v155, v156, v155
	v_mul_f32_e32 v156, 0xbfb8aa3b, v155
	v_exp_f32_e32 v156, v156
	s_nop 0
	v_add_f32_e32 v156, 1.0, v156
	v_rcp_f32_e32 v156, v156
	s_nop 0
	v_mul_f32_e32 v155, v155, v156
	v_cvt_f32_i32_e32 v156, v132
	v_mul_f32_e32 v156, v157, v156
	v_mul_f32_e32 v157, 0xbfb8aa3b, v156
	v_exp_f32_e32 v157, v157
	s_nop 0
	v_add_f32_e32 v157, 1.0, v157
	v_rcp_f32_e32 v157, v157
	s_nop 0
	v_mul_f32_e32 v158, v156, v157
	v_cvt_f32_i32_e32 v156, v133
	v_mul_f32_e32 v157, v33, v148
	v_mul_f32_e32 v156, v157, v156
	v_mul_f32_e32 v157, 0xbfb8aa3b, v156
	v_exp_f32_e32 v157, v157
	s_nop 0
	v_add_f32_e32 v157, 1.0, v157
	v_rcp_f32_e32 v157, v157
	s_nop 0
	v_mul_f32_e32 v159, v156, v157
	v_cvt_f32_i32_e32 v156, v134
	v_mul_f32_e32 v157, v34, v148
	v_mul_f32_e32 v156, v157, v156
	v_mul_f32_e32 v157, 0xbfb8aa3b, v156
	v_exp_f32_e32 v157, v157
	s_nop 0
	v_add_f32_e32 v157, 1.0, v157
	v_rcp_f32_e32 v157, v157
	s_nop 0
	v_mul_f32_e32 v165, v156, v157
	v_cvt_f32_i32_e32 v156, v135
	v_mul_f32_e32 v157, v35, v148
	v_mul_f32_e32 v156, v157, v156
	v_mul_f32_e32 v157, 0xbfb8aa3b, v156
	v_exp_f32_e32 v157, v157
	s_nop 0
	v_add_f32_e32 v157, 1.0, v157
	v_rcp_f32_e32 v157, v157
	s_nop 0
	v_mul_f32_e32 v166, v156, v157
	v_cvt_pk_bf16_f32 v156, v145, v152
	v_cvt_f32_i32_e32 v145, v136
	v_cvt_pk_bf16_f32 v157, v153, v155
	v_mul_f32_e32 v155, v44, v148
	v_lshl_add_u64 v[152:153], v[146:147], 0, s[72:73]
	v_mul_f32_e32 v145, v155, v145
	v_mul_f32_e32 v155, 0xbfb8aa3b, v145
	v_exp_f32_e32 v155, v155
	v_lshlrev_b64 v[146:147], 1, v[150:151]
	v_lshl_add_u64 v[152:153], v[152:153], 0, v[146:147]
	v_cvt_pk_bf16_f32 v158, v158, v159
	v_add_f32_e32 v155, 1.0, v155
	v_rcp_f32_e32 v155, v155
	v_cvt_pk_bf16_f32 v159, v165, v166
	global_store_dwordx4 v[152:153], v[156:159], off
	v_mul_f32_e32 v165, v37, v148
	v_mul_f32_e32 v145, v145, v155
	v_cvt_f32_i32_e32 v155, v137
	v_mul_f32_e32 v156, v45, v148
	v_mul_f32_e32 v157, v46, v148
	v_mul_f32_e32 v158, v47, v148
	v_mul_f32_e32 v155, v156, v155
	v_mul_f32_e32 v156, 0xbfb8aa3b, v155
	v_exp_f32_e32 v156, v156
	v_mul_f32_e32 v159, v36, v148
	v_mul_f32_e32 v166, v38, v148
	v_mul_f32_e32 v148, v39, v148
	v_add_f32_e32 v156, 1.0, v156
	v_rcp_f32_e32 v156, v156
	s_nop 0
	v_mul_f32_e32 v155, v155, v156
	v_cvt_f32_i32_e32 v156, v138
	v_mul_f32_e32 v156, v157, v156
	v_mul_f32_e32 v157, 0xbfb8aa3b, v156
	v_exp_f32_e32 v157, v157
	s_nop 0
	v_add_f32_e32 v157, 1.0, v157
	v_rcp_f32_e32 v157, v157
	s_nop 0
	v_mul_f32_e32 v157, v156, v157
	v_cvt_f32_i32_e32 v156, v139
	v_mul_f32_e32 v156, v158, v156
	v_mul_f32_e32 v158, 0xbfb8aa3b, v156
	v_exp_f32_e32 v158, v158
	s_nop 0
	v_add_f32_e32 v158, 1.0, v158
	v_rcp_f32_e32 v158, v158
	s_nop 0
	v_mul_f32_e32 v158, v156, v158
	v_cvt_f32_i32_e32 v156, v128
	v_mul_f32_e32 v156, v159, v156
	v_mul_f32_e32 v159, 0xbfb8aa3b, v156
	v_exp_f32_e32 v159, v159
	s_nop 0
	v_add_f32_e32 v159, 1.0, v159
	v_rcp_f32_e32 v159, v159
	s_nop 0
	v_mul_f32_e32 v159, v156, v159
	v_cvt_f32_i32_e32 v156, v129
	v_mul_f32_e32 v156, v165, v156
	v_mul_f32_e32 v165, 0xbfb8aa3b, v156
	v_exp_f32_e32 v165, v165
	s_nop 0
	v_add_f32_e32 v165, 1.0, v165
	v_rcp_f32_e32 v165, v165
	s_nop 0
	v_mul_f32_e32 v165, v156, v165
	v_cvt_f32_i32_e32 v156, v130
	v_mul_f32_e32 v156, v166, v156
	v_mul_f32_e32 v166, 0xbfb8aa3b, v156
	v_exp_f32_e32 v166, v166
	s_nop 0
	v_add_f32_e32 v166, 1.0, v166
	v_rcp_f32_e32 v166, v166
	s_nop 0
	v_mul_f32_e32 v166, v156, v166
; #define GAS __attribute__((address_space(1)))
; __device__ __forceinline__ v4u pack8(const f32x4 a, const f32x4 b) { v4u w; w.x = cvt_pk_bf16(a[0], a[1]); w.y = cvt_pk_bf16(a[2], a[3]); w.z = cvt_pk_bf16(b[0], b[1]); w.w = cvt_pk_bf16(b[2], b[3]); return w; }
; __device__ __forceinline__ float fexp(float x) { return __builtin_amdgcn_exp2f(x * 1.4426950408889634f); }
; #define EPI_LOOP_AM for (int ai = 0; ai < 2; ++ai) _Pragma("unroll") for (int m = 0; m < 4; ++m)
;     __device__ __forceinline__ void operator()(AccI& acci, const Unit& u, LAS unsigned char*, int wr, int wc, int fr, int fq) const {
;     ...
;             EPI_LOOP_AM {
;                 const int r = 128 * ai + 64 * wr + 16 * m + fr, tok = pm * 256 + r; const float sxr = sx0[tok];
; #pragma unroll
;                 for (int bj = 0; bj < 2; ++bj) { f32x4 v[2];
; #pragma unroll
;                     for (int n = 0; n < 2; ++n)
; #pragma unroll
;                         for (int j = 0; j < 4; ++j) { const float g = ACCF(ai, bj, m, n, j); v[n][j] = g * __builtin_amdgcn_rcpf(1.f + fexp(-g)); }
;                     *(GAS v4u*)(gs + (size_t)tok * RW + (pn - 8) * 256 + bj * 128 + c0) = pack8(v[0], v[1]); }
	v_cvt_f32_i32_e32 v156, v131
	v_mul_f32_e32 v148, v148, v156
	v_mul_f32_e32 v156, 0xbfb8aa3b, v148
	v_exp_f32_e32 v156, v156
	s_nop 0
	v_add_f32_e32 v156, 1.0, v156
	v_rcp_f32_e32 v156, v156
	s_nop 0
	v_mul_f32_e32 v148, v148, v156
	v_cvt_pk_bf16_f32 v156, v145, v155
	v_cvt_pk_bf16_f32 v157, v157, v158
	v_cvt_pk_bf16_f32 v158, v159, v165
	v_cvt_pk_bf16_f32 v159, v166, v148
	global_store_dwordx4 v[152:153], v[156:159], off offset:256
	v_add_u32_e32 v152, 16, v144
	v_ashrrev_i32_e32 v153, 31, v152
	v_lshl_add_u64 v[156:157], v[152:153], 2, s[34:35]
	v_mov_b32_e32 v145, v216
	v_cvt_f32_i32_e32 v148, v124
	v_lshlrev_b64 v[152:153], 11, v[152:153]
	v_lshl_add_u64 v[152:153], s[42:43], 0, v[152:153]
	v_lshl_add_u64 v[152:153], v[152:153], 0, s[72:73]
	v_lshl_add_u64 v[152:153], v[152:153], 0, v[146:147]
	v_mul_f32_e32 v155, v40, v145
	v_mul_f32_e32 v148, v155, v148
	v_mul_f32_e32 v155, 0xbfb8aa3b, v148
	v_exp_f32_e32 v155, v155
	v_mul_f32_e32 v156, v41, v145
	v_mul_f32_e32 v157, v42, v145
	v_mul_f32_e32 v158, v43, v145
	v_add_f32_e32 v155, 1.0, v155
	v_rcp_f32_e32 v155, v155
	v_mul_f32_e32 v159, v32, v145
	v_mul_f32_e32 v165, v33, v145
	v_mul_f32_e32 v166, v34, v145
	v_mul_f32_e32 v148, v148, v155
	v_cvt_f32_i32_e32 v155, v125
	v_mul_f32_e32 v167, v35, v145
	v_mul_f32_e32 v155, v156, v155
	v_mul_f32_e32 v156, 0xbfb8aa3b, v155
	v_exp_f32_e32 v156, v156
	s_nop 0
	v_add_f32_e32 v156, 1.0, v156
	v_rcp_f32_e32 v156, v156
	s_nop 0
	v_mul_f32_e32 v155, v155, v156
	v_cvt_f32_i32_e32 v156, v126
	v_mul_f32_e32 v156, v157, v156
	v_mul_f32_e32 v157, 0xbfb8aa3b, v156
	v_exp_f32_e32 v157, v157
	s_nop 0
	v_add_f32_e32 v157, 1.0, v157
	v_rcp_f32_e32 v157, v157
	s_nop 0
	v_mul_f32_e32 v157, v156, v157
	v_cvt_f32_i32_e32 v156, v127
	v_mul_f32_e32 v156, v158, v156
	v_mul_f32_e32 v158, 0xbfb8aa3b, v156
	v_exp_f32_e32 v158, v158
	s_nop 0
	v_add_f32_e32 v158, 1.0, v158
	v_rcp_f32_e32 v158, v158
	s_nop 0
	v_mul_f32_e32 v158, v156, v158
	v_cvt_f32_i32_e32 v156, v116
	v_mul_f32_e32 v156, v159, v156
	v_mul_f32_e32 v159, 0xbfb8aa3b, v156
	v_exp_f32_e32 v159, v159
	s_nop 0
	v_add_f32_e32 v159, 1.0, v159
	v_rcp_f32_e32 v159, v159
	s_nop 0
	v_mul_f32_e32 v159, v156, v159
	v_cvt_f32_i32_e32 v156, v117
	v_mul_f32_e32 v156, v165, v156
	v_mul_f32_e32 v165, 0xbfb8aa3b, v156
	v_exp_f32_e32 v165, v165
	s_nop 0
	v_add_f32_e32 v165, 1.0, v165
	v_rcp_f32_e32 v165, v165
	s_nop 0
	v_mul_f32_e32 v165, v156, v165
	v_cvt_f32_i32_e32 v156, v118
	v_mul_f32_e32 v156, v166, v156
	v_mul_f32_e32 v166, 0xbfb8aa3b, v156
	v_exp_f32_e32 v166, v166
	s_nop 0
	v_add_f32_e32 v166, 1.0, v166
	v_rcp_f32_e32 v166, v166
	s_nop 0
	v_mul_f32_e32 v166, v156, v166
	v_cvt_f32_i32_e32 v156, v119
	v_mul_f32_e32 v156, v167, v156
	v_mul_f32_e32 v167, 0xbfb8aa3b, v156
	v_exp_f32_e32 v167, v167
	s_nop 0
	v_add_f32_e32 v167, 1.0, v167
	v_rcp_f32_e32 v167, v167
	s_nop 0
	v_mul_f32_e32 v167, v156, v167
	v_cvt_pk_bf16_f32 v156, v148, v155
	v_cvt_f32_i32_e32 v148, v120
	v_mul_f32_e32 v155, v44, v145
	v_cvt_pk_bf16_f32 v157, v157, v158
	v_cvt_pk_bf16_f32 v158, v159, v165
	v_mul_f32_e32 v148, v155, v148
	v_mul_f32_e32 v155, 0xbfb8aa3b, v148
	v_exp_f32_e32 v155, v155
	v_cvt_pk_bf16_f32 v159, v166, v167
	global_store_dwordx4 v[152:153], v[156:159], off
	v_mul_f32_e32 v165, v37, v145
	v_add_f32_e32 v155, 1.0, v155
	v_rcp_f32_e32 v155, v155
	v_mul_f32_e32 v156, v45, v145
	v_mul_f32_e32 v157, v46, v145
	v_mul_f32_e32 v158, v47, v145
	v_mul_f32_e32 v148, v148, v155
	v_cvt_f32_i32_e32 v155, v121
	v_mul_f32_e32 v159, v36, v145
	v_mul_f32_e32 v166, v38, v145
	v_mul_f32_e32 v145, v39, v145
	v_mul_f32_e32 v155, v156, v155
	v_mul_f32_e32 v156, 0xbfb8aa3b, v155
	v_exp_f32_e32 v156, v156
	s_nop 0
	v_add_f32_e32 v156, 1.0, v156
	v_rcp_f32_e32 v156, v156
	s_nop 0
	v_mul_f32_e32 v155, v155, v156
	v_cvt_f32_i32_e32 v156, v122
	v_mul_f32_e32 v156, v157, v156
	v_mul_f32_e32 v157, 0xbfb8aa3b, v156
	v_exp_f32_e32 v157, v157
	s_nop 0
	v_add_f32_e32 v157, 1.0, v157
	v_rcp_f32_e32 v157, v157
	s_nop 0
	v_mul_f32_e32 v157, v156, v157
	v_cvt_f32_i32_e32 v156, v123
	v_mul_f32_e32 v156, v158, v156
	v_mul_f32_e32 v158, 0xbfb8aa3b, v156
	v_exp_f32_e32 v158, v158
	s_nop 0
	v_add_f32_e32 v158, 1.0, v158
	v_rcp_f32_e32 v158, v158
	s_nop 0
	v_mul_f32_e32 v158, v156, v158
	v_cvt_f32_i32_e32 v156, v112
	v_mul_f32_e32 v156, v159, v156
	v_mul_f32_e32 v159, 0xbfb8aa3b, v156
	v_exp_f32_e32 v159, v159
	s_nop 0
	v_add_f32_e32 v159, 1.0, v159
	v_rcp_f32_e32 v159, v159
	s_nop 0
	v_mul_f32_e32 v159, v156, v159
	v_cvt_f32_i32_e32 v156, v113
	v_mul_f32_e32 v156, v165, v156
	v_mul_f32_e32 v165, 0xbfb8aa3b, v156
	v_exp_f32_e32 v165, v165
	s_nop 0
	v_add_f32_e32 v165, 1.0, v165
	v_rcp_f32_e32 v165, v165
	s_nop 0
	v_mul_f32_e32 v165, v156, v165
	v_cvt_f32_i32_e32 v156, v114
	v_mul_f32_e32 v156, v166, v156
	v_mul_f32_e32 v166, 0xbfb8aa3b, v156
	v_exp_f32_e32 v166, v166
	s_nop 0
	v_add_f32_e32 v166, 1.0, v166
	v_rcp_f32_e32 v166, v166
	s_nop 0
	v_mul_f32_e32 v166, v156, v166
	v_cvt_f32_i32_e32 v156, v115
	v_mul_f32_e32 v145, v145, v156
	v_mul_f32_e32 v156, 0xbfb8aa3b, v145
	v_exp_f32_e32 v156, v156
	s_nop 0
	v_add_f32_e32 v156, 1.0, v156
	v_rcp_f32_e32 v156, v156
	s_nop 0
	v_mul_f32_e32 v145, v145, v156
	v_cvt_pk_bf16_f32 v156, v148, v155
	v_cvt_pk_bf16_f32 v157, v157, v158
	v_cvt_pk_bf16_f32 v158, v159, v165
	v_cvt_pk_bf16_f32 v159, v166, v145
	global_store_dwordx4 v[152:153], v[156:159], off offset:256
	v_add_u32_e32 v152, 32, v144
	v_ashrrev_i32_e32 v153, 31, v152
	v_lshl_add_u64 v[156:157], v[152:153], 2, s[34:35]
	v_mov_b32_e32 v145, v217
	v_cvt_f32_i32_e32 v148, v108
	v_lshlrev_b64 v[152:153], 11, v[152:153]
	v_lshl_add_u64 v[152:153], s[42:43], 0, v[152:153]
; #define GAS __attribute__((address_space(1)))
; __device__ __forceinline__ v4u pack8(const f32x4 a, const f32x4 b) { v4u w; w.x = cvt_pk_bf16(a[0], a[1]); w.y = cvt_pk_bf16(a[2], a[3]); w.z = cvt_pk_bf16(b[0], b[1]); w.w = cvt_pk_bf16(b[2], b[3]); return w; }
; __device__ __forceinline__ float fexp(float x) { return __builtin_amdgcn_exp2f(x * 1.4426950408889634f); }
; #define EPI_LOOP_AM for (int ai = 0; ai < 2; ++ai) _Pragma("unroll") for (int m = 0; m < 4; ++m)
;     __device__ __forceinline__ void operator()(AccI& acci, const Unit& u, LAS unsigned char*, int wr, int wc, int fr, int fq) const {
;     ...
;             EPI_LOOP_AM {
;                 const int r = 128 * ai + 64 * wr + 16 * m + fr, tok = pm * 256 + r; const float sxr = sx0[tok];
; #pragma unroll
;                 for (int bj = 0; bj < 2; ++bj) { f32x4 v[2];
; #pragma unroll
;                     for (int n = 0; n < 2; ++n)
; #pragma unroll
;                         for (int j = 0; j < 4; ++j) { const float g = ACCF(ai, bj, m, n, j); v[n][j] = g * __builtin_amdgcn_rcpf(1.f + fexp(-g)); }
;                     *(GAS v4u*)(gs + (size_t)tok * RW + (pn - 8) * 256 + bj * 128 + c0) = pack8(v[0], v[1]); }
	v_lshl_add_u64 v[152:153], v[152:153], 0, s[72:73]
	v_lshl_add_u64 v[152:153], v[152:153], 0, v[146:147]
	v_mul_f32_e32 v155, v40, v145
	v_mul_f32_e32 v148, v155, v148
	v_mul_f32_e32 v155, 0xbfb8aa3b, v148
	v_exp_f32_e32 v155, v155
	v_mul_f32_e32 v156, v41, v145
	v_mul_f32_e32 v157, v42, v145
	v_mul_f32_e32 v158, v43, v145
	v_add_f32_e32 v155, 1.0, v155
	v_rcp_f32_e32 v155, v155
	v_mul_f32_e32 v159, v32, v145
	v_mul_f32_e32 v165, v33, v145
	v_mul_f32_e32 v166, v34, v145
	v_mul_f32_e32 v148, v148, v155
	v_cvt_f32_i32_e32 v155, v109
	v_mul_f32_e32 v167, v35, v145
	v_mul_f32_e32 v155, v156, v155
	v_mul_f32_e32 v156, 0xbfb8aa3b, v155
	v_exp_f32_e32 v156, v156
	s_nop 0
	v_add_f32_e32 v156, 1.0, v156
	v_rcp_f32_e32 v156, v156
	s_nop 0
	v_mul_f32_e32 v155, v155, v156
	v_cvt_f32_i32_e32 v156, v110
	v_mul_f32_e32 v156, v157, v156
	v_mul_f32_e32 v157, 0xbfb8aa3b, v156
	v_exp_f32_e32 v157, v157
	s_nop 0
	v_add_f32_e32 v157, 1.0, v157
	v_rcp_f32_e32 v157, v157
	s_nop 0
	v_mul_f32_e32 v157, v156, v157
	v_cvt_f32_i32_e32 v156, v111
	v_mul_f32_e32 v156, v158, v156
	v_mul_f32_e32 v158, 0xbfb8aa3b, v156
	v_exp_f32_e32 v158, v158
	s_nop 0
	v_add_f32_e32 v158, 1.0, v158
	v_rcp_f32_e32 v158, v158
	s_nop 0
	v_mul_f32_e32 v158, v156, v158
	v_cvt_f32_i32_e32 v156, v100
	v_mul_f32_e32 v156, v159, v156
	v_mul_f32_e32 v159, 0xbfb8aa3b, v156
	v_exp_f32_e32 v159, v159
	s_nop 0
	v_add_f32_e32 v159, 1.0, v159
	v_rcp_f32_e32 v159, v159
	s_nop 0
	v_mul_f32_e32 v159, v156, v159
	v_cvt_f32_i32_e32 v156, v101
	v_mul_f32_e32 v156, v165, v156
	v_mul_f32_e32 v165, 0xbfb8aa3b, v156
	v_exp_f32_e32 v165, v165
	s_nop 0
	v_add_f32_e32 v165, 1.0, v165
	v_rcp_f32_e32 v165, v165
	s_nop 0
	v_mul_f32_e32 v165, v156, v165
	v_cvt_f32_i32_e32 v156, v102
	v_mul_f32_e32 v156, v166, v156
	v_mul_f32_e32 v166, 0xbfb8aa3b, v156
	v_exp_f32_e32 v166, v166
	s_nop 0
	v_add_f32_e32 v166, 1.0, v166
	v_rcp_f32_e32 v166, v166
	s_nop 0
	v_mul_f32_e32 v166, v156, v166
	v_cvt_f32_i32_e32 v156, v103
	v_mul_f32_e32 v156, v167, v156
	v_mul_f32_e32 v167, 0xbfb8aa3b, v156
	v_exp_f32_e32 v167, v167
	s_nop 0
	v_add_f32_e32 v167, 1.0, v167
	v_rcp_f32_e32 v167, v167
	s_nop 0
	v_mul_f32_e32 v167, v156, v167
	v_cvt_pk_bf16_f32 v156, v148, v155
	v_cvt_f32_i32_e32 v148, v104
	v_mul_f32_e32 v155, v44, v145
	v_cvt_pk_bf16_f32 v157, v157, v158
	v_cvt_pk_bf16_f32 v158, v159, v165
	v_mul_f32_e32 v148, v155, v148
	v_mul_f32_e32 v155, 0xbfb8aa3b, v148
	v_exp_f32_e32 v155, v155
	v_cvt_pk_bf16_f32 v159, v166, v167
	global_store_dwordx4 v[152:153], v[156:159], off
	v_mul_f32_e32 v165, v37, v145
	v_add_f32_e32 v155, 1.0, v155
	v_rcp_f32_e32 v155, v155
	v_mul_f32_e32 v156, v45, v145
	v_mul_f32_e32 v157, v46, v145
	v_mul_f32_e32 v158, v47, v145
	v_mul_f32_e32 v148, v148, v155
	v_cvt_f32_i32_e32 v155, v105
	v_mul_f32_e32 v159, v36, v145
	v_mul_f32_e32 v166, v38, v145
	v_mul_f32_e32 v145, v39, v145
	v_mul_f32_e32 v155, v156, v155
	v_mul_f32_e32 v156, 0xbfb8aa3b, v155
	v_exp_f32_e32 v156, v156
	s_nop 0
	v_add_f32_e32 v156, 1.0, v156
	v_rcp_f32_e32 v156, v156
	s_nop 0
	v_mul_f32_e32 v155, v155, v156
	v_cvt_f32_i32_e32 v156, v106
	v_mul_f32_e32 v156, v157, v156
	v_mul_f32_e32 v157, 0xbfb8aa3b, v156
	v_exp_f32_e32 v157, v157
	s_nop 0
	v_add_f32_e32 v157, 1.0, v157
	v_rcp_f32_e32 v157, v157
	s_nop 0
	v_mul_f32_e32 v157, v156, v157
	v_cvt_f32_i32_e32 v156, v107
	v_mul_f32_e32 v156, v158, v156
	v_mul_f32_e32 v158, 0xbfb8aa3b, v156
	v_exp_f32_e32 v158, v158
	s_nop 0
	v_add_f32_e32 v158, 1.0, v158
	v_rcp_f32_e32 v158, v158
	s_nop 0
	v_mul_f32_e32 v158, v156, v158
	v_cvt_f32_i32_e32 v156, v96
	v_mul_f32_e32 v156, v159, v156
	v_mul_f32_e32 v159, 0xbfb8aa3b, v156
	v_exp_f32_e32 v159, v159
	s_nop 0
	v_add_f32_e32 v159, 1.0, v159
	v_rcp_f32_e32 v159, v159
	s_nop 0
	v_mul_f32_e32 v159, v156, v159
	v_cvt_f32_i32_e32 v156, v97
	v_mul_f32_e32 v156, v165, v156
	v_mul_f32_e32 v165, 0xbfb8aa3b, v156
	v_exp_f32_e32 v165, v165
	s_nop 0
	v_add_f32_e32 v165, 1.0, v165
	v_rcp_f32_e32 v165, v165
	s_nop 0
	v_mul_f32_e32 v165, v156, v165
	v_cvt_f32_i32_e32 v156, v98
	v_mul_f32_e32 v156, v166, v156
	v_mul_f32_e32 v166, 0xbfb8aa3b, v156
	v_exp_f32_e32 v166, v166
	s_nop 0
	v_add_f32_e32 v166, 1.0, v166
	v_rcp_f32_e32 v166, v166
	s_nop 0
	v_mul_f32_e32 v166, v156, v166
	v_cvt_f32_i32_e32 v156, v99
	v_mul_f32_e32 v145, v145, v156
	v_mul_f32_e32 v156, 0xbfb8aa3b, v145
	v_exp_f32_e32 v156, v156
	s_nop 0
	v_add_f32_e32 v156, 1.0, v156
	v_rcp_f32_e32 v156, v156
	s_nop 0
	v_mul_f32_e32 v145, v145, v156
	v_cvt_pk_bf16_f32 v156, v148, v155
	v_cvt_pk_bf16_f32 v157, v157, v158
	v_cvt_pk_bf16_f32 v158, v159, v165
	v_cvt_pk_bf16_f32 v159, v166, v145
	global_store_dwordx4 v[152:153], v[156:159], off offset:256
	v_add_u32_e32 v152, 48, v144
	v_ashrrev_i32_e32 v153, 31, v152
	v_lshl_add_u64 v[156:157], v[152:153], 2, s[34:35]
	v_mov_b32_e32 v145, v218
	v_cvt_f32_i32_e32 v148, v92
	v_lshlrev_b64 v[152:153], 11, v[152:153]
	v_lshl_add_u64 v[152:153], s[42:43], 0, v[152:153]
	v_lshl_add_u64 v[152:153], v[152:153], 0, s[72:73]
	v_lshl_add_u64 v[152:153], v[152:153], 0, v[146:147]
	v_mul_f32_e32 v155, v40, v145
	v_mul_f32_e32 v148, v155, v148
	v_mul_f32_e32 v155, 0xbfb8aa3b, v148
	v_exp_f32_e32 v155, v155
	v_mul_f32_e32 v156, v41, v145
	v_mul_f32_e32 v157, v42, v145
	v_mul_f32_e32 v158, v43, v145
	v_add_f32_e32 v155, 1.0, v155
	v_rcp_f32_e32 v155, v155
	v_mul_f32_e32 v159, v32, v145
	v_mul_f32_e32 v165, v33, v145
	v_mul_f32_e32 v166, v34, v145
	v_mul_f32_e32 v148, v148, v155
	v_cvt_f32_i32_e32 v155, v93
	v_mul_f32_e32 v167, v35, v145
	v_mul_f32_e32 v155, v156, v155
	v_mul_f32_e32 v156, 0xbfb8aa3b, v155
	v_exp_f32_e32 v156, v156
	s_nop 0
	v_add_f32_e32 v156, 1.0, v156
; #define GAS __attribute__((address_space(1)))
; __device__ __forceinline__ v4u pack8(const f32x4 a, const f32x4 b) { v4u w; w.x = cvt_pk_bf16(a[0], a[1]); w.y = cvt_pk_bf16(a[2], a[3]); w.z = cvt_pk_bf16(b[0], b[1]); w.w = cvt_pk_bf16(b[2], b[3]); return w; }
; __device__ __forceinline__ float fexp(float x) { return __builtin_amdgcn_exp2f(x * 1.4426950408889634f); }
; #define EPI_LOOP_AM for (int ai = 0; ai < 2; ++ai) _Pragma("unroll") for (int m = 0; m < 4; ++m)
;     __device__ __forceinline__ void operator()(AccI& acci, const Unit& u, LAS unsigned char*, int wr, int wc, int fr, int fq) const {
;     ...
;             EPI_LOOP_AM {
;                 const int r = 128 * ai + 64 * wr + 16 * m + fr, tok = pm * 256 + r; const float sxr = sx0[tok];
; #pragma unroll
;                 for (int bj = 0; bj < 2; ++bj) { f32x4 v[2];
; #pragma unroll
;                     for (int n = 0; n < 2; ++n)
; #pragma unroll
;                         for (int j = 0; j < 4; ++j) { const float g = ACCF(ai, bj, m, n, j); v[n][j] = g * __builtin_amdgcn_rcpf(1.f + fexp(-g)); }
;                     *(GAS v4u*)(gs + (size_t)tok * RW + (pn - 8) * 256 + bj * 128 + c0) = pack8(v[0], v[1]); }
	v_rcp_f32_e32 v156, v156
	s_nop 0
	v_mul_f32_e32 v155, v155, v156
	v_cvt_f32_i32_e32 v156, v94
	v_mul_f32_e32 v156, v157, v156
	v_mul_f32_e32 v157, 0xbfb8aa3b, v156
	v_exp_f32_e32 v157, v157
	s_nop 0
	v_add_f32_e32 v157, 1.0, v157
	v_rcp_f32_e32 v157, v157
	s_nop 0
	v_mul_f32_e32 v157, v156, v157
	v_cvt_f32_i32_e32 v156, v95
	v_mul_f32_e32 v156, v158, v156
	v_mul_f32_e32 v158, 0xbfb8aa3b, v156
	v_exp_f32_e32 v158, v158
	s_nop 0
	v_add_f32_e32 v158, 1.0, v158
	v_rcp_f32_e32 v158, v158
	s_nop 0
	v_mul_f32_e32 v158, v156, v158
	v_cvt_f32_i32_e32 v156, v84
	v_mul_f32_e32 v156, v159, v156
	v_mul_f32_e32 v159, 0xbfb8aa3b, v156
	v_exp_f32_e32 v159, v159
	s_nop 0
	v_add_f32_e32 v159, 1.0, v159
	v_rcp_f32_e32 v159, v159
	s_nop 0
	v_mul_f32_e32 v159, v156, v159
	v_cvt_f32_i32_e32 v156, v85
	v_mul_f32_e32 v156, v165, v156
	v_mul_f32_e32 v165, 0xbfb8aa3b, v156
	v_exp_f32_e32 v165, v165
	s_nop 0
	v_add_f32_e32 v165, 1.0, v165
	v_rcp_f32_e32 v165, v165
	s_nop 0
	v_mul_f32_e32 v165, v156, v165
	v_cvt_f32_i32_e32 v156, v86
	v_mul_f32_e32 v156, v166, v156
	v_mul_f32_e32 v166, 0xbfb8aa3b, v156
	v_exp_f32_e32 v166, v166
	s_nop 0
	v_add_f32_e32 v166, 1.0, v166
	v_rcp_f32_e32 v166, v166
	s_nop 0
	v_mul_f32_e32 v166, v156, v166
	v_cvt_f32_i32_e32 v156, v87
	v_mul_f32_e32 v156, v167, v156
	v_mul_f32_e32 v167, 0xbfb8aa3b, v156
	v_exp_f32_e32 v167, v167
	s_nop 0
	v_add_f32_e32 v167, 1.0, v167
	v_rcp_f32_e32 v167, v167
	s_nop 0
	v_mul_f32_e32 v167, v156, v167
	v_cvt_pk_bf16_f32 v156, v148, v155
	v_cvt_f32_i32_e32 v148, v88
	v_mul_f32_e32 v155, v44, v145
	v_cvt_pk_bf16_f32 v157, v157, v158
	v_cvt_pk_bf16_f32 v158, v159, v165
	v_mul_f32_e32 v148, v155, v148
	v_mul_f32_e32 v155, 0xbfb8aa3b, v148
	v_exp_f32_e32 v155, v155
	v_cvt_pk_bf16_f32 v159, v166, v167
	global_store_dwordx4 v[152:153], v[156:159], off
	v_mul_f32_e32 v165, v37, v145
	v_add_f32_e32 v155, 1.0, v155
	v_rcp_f32_e32 v155, v155
	v_mul_f32_e32 v156, v45, v145
	v_mul_f32_e32 v157, v46, v145
	v_mul_f32_e32 v158, v47, v145
	v_mul_f32_e32 v148, v148, v155
	v_cvt_f32_i32_e32 v155, v89
	v_mul_f32_e32 v159, v36, v145
	v_mul_f32_e32 v166, v38, v145
	v_mul_f32_e32 v145, v39, v145
	v_mul_f32_e32 v155, v156, v155
	v_mul_f32_e32 v156, 0xbfb8aa3b, v155
	v_exp_f32_e32 v156, v156
	s_nop 0
	v_add_f32_e32 v156, 1.0, v156
	v_rcp_f32_e32 v156, v156
	s_nop 0
	v_mul_f32_e32 v155, v155, v156
	v_cvt_f32_i32_e32 v156, v90
	v_mul_f32_e32 v156, v157, v156
	v_mul_f32_e32 v157, 0xbfb8aa3b, v156
	v_exp_f32_e32 v157, v157
	s_nop 0
	v_add_f32_e32 v157, 1.0, v157
	v_rcp_f32_e32 v157, v157
	s_nop 0
	v_mul_f32_e32 v157, v156, v157
	v_cvt_f32_i32_e32 v156, v91
	v_mul_f32_e32 v156, v158, v156
	v_mul_f32_e32 v158, 0xbfb8aa3b, v156
	v_exp_f32_e32 v158, v158
	s_nop 0
	v_add_f32_e32 v158, 1.0, v158
	v_rcp_f32_e32 v158, v158
	s_nop 0
	v_mul_f32_e32 v158, v156, v158
	v_cvt_f32_i32_e32 v156, v80
	v_mul_f32_e32 v156, v159, v156
	v_mul_f32_e32 v159, 0xbfb8aa3b, v156
	v_exp_f32_e32 v159, v159
	s_nop 0
	v_add_f32_e32 v159, 1.0, v159
	v_rcp_f32_e32 v159, v159
	s_nop 0
	v_mul_f32_e32 v159, v156, v159
	v_cvt_f32_i32_e32 v156, v81
	v_mul_f32_e32 v156, v165, v156
	v_mul_f32_e32 v165, 0xbfb8aa3b, v156
	v_exp_f32_e32 v165, v165
	s_nop 0
	v_add_f32_e32 v165, 1.0, v165
	v_rcp_f32_e32 v165, v165
	s_nop 0
	v_mul_f32_e32 v165, v156, v165
	v_cvt_f32_i32_e32 v156, v82
	v_mul_f32_e32 v156, v166, v156
	v_mul_f32_e32 v166, 0xbfb8aa3b, v156
	v_exp_f32_e32 v166, v166
	s_nop 0
	v_add_f32_e32 v166, 1.0, v166
	v_rcp_f32_e32 v166, v166
	s_nop 0
	v_mul_f32_e32 v166, v156, v166
	v_cvt_f32_i32_e32 v156, v83
	v_mul_f32_e32 v145, v145, v156
	v_mul_f32_e32 v156, 0xbfb8aa3b, v145
	v_exp_f32_e32 v156, v156
	s_nop 0
	v_add_f32_e32 v156, 1.0, v156
	v_rcp_f32_e32 v156, v156
	s_nop 0
	v_mul_f32_e32 v145, v145, v156
	v_cvt_pk_bf16_f32 v156, v148, v155
	v_cvt_pk_bf16_f32 v157, v157, v158
	v_cvt_pk_bf16_f32 v158, v159, v165
	v_cvt_pk_bf16_f32 v159, v166, v145
	global_store_dwordx4 v[152:153], v[156:159], off offset:256
	v_add_u32_e32 v152, 0x80, v144
	v_ashrrev_i32_e32 v153, 31, v152
	v_lshl_add_u64 v[156:157], v[152:153], 2, s[34:35]
	v_mov_b32_e32 v145, v219
	v_cvt_f32_i32_e32 v148, v76
	v_lshlrev_b64 v[152:153], 11, v[152:153]
	v_lshl_add_u64 v[152:153], s[42:43], 0, v[152:153]
	v_lshl_add_u64 v[152:153], v[152:153], 0, s[72:73]
	v_lshl_add_u64 v[152:153], v[152:153], 0, v[146:147]
	v_mul_f32_e32 v155, v40, v145
	v_mul_f32_e32 v148, v155, v148
	v_mul_f32_e32 v155, 0xbfb8aa3b, v148
	v_exp_f32_e32 v155, v155
	v_mul_f32_e32 v156, v41, v145
	v_mul_f32_e32 v157, v42, v145
	v_mul_f32_e32 v158, v43, v145
	v_add_f32_e32 v155, 1.0, v155
	v_rcp_f32_e32 v155, v155
	v_mul_f32_e32 v159, v32, v145
	v_mul_f32_e32 v165, v33, v145
	v_mul_f32_e32 v166, v34, v145
	v_mul_f32_e32 v148, v148, v155
	v_cvt_f32_i32_e32 v155, v77
	v_mul_f32_e32 v167, v35, v145
	v_mul_f32_e32 v155, v156, v155
	v_mul_f32_e32 v156, 0xbfb8aa3b, v155
	v_exp_f32_e32 v156, v156
	s_nop 0
	v_add_f32_e32 v156, 1.0, v156
	v_rcp_f32_e32 v156, v156
	s_nop 0
	v_mul_f32_e32 v155, v155, v156
	v_cvt_f32_i32_e32 v156, v78
	v_mul_f32_e32 v156, v157, v156
	v_mul_f32_e32 v157, 0xbfb8aa3b, v156
	v_exp_f32_e32 v157, v157
	s_nop 0
	v_add_f32_e32 v157, 1.0, v157
	v_rcp_f32_e32 v157, v157
	s_nop 0
	v_mul_f32_e32 v157, v156, v157
	v_cvt_f32_i32_e32 v156, v79
	v_mul_f32_e32 v156, v158, v156
	v_mul_f32_e32 v158, 0xbfb8aa3b, v156
	v_exp_f32_e32 v158, v158
	s_nop 0
	v_add_f32_e32 v158, 1.0, v158
	v_rcp_f32_e32 v158, v158
	s_nop 0
	v_mul_f32_e32 v158, v156, v158
	v_cvt_f32_i32_e32 v156, v68
	v_mul_f32_e32 v156, v159, v156
	v_mul_f32_e32 v159, 0xbfb8aa3b, v156
	v_exp_f32_e32 v159, v159
	s_nop 0
	v_add_f32_e32 v159, 1.0, v159
	v_rcp_f32_e32 v159, v159
; #define GAS __attribute__((address_space(1)))
; __device__ __forceinline__ v4u pack8(const f32x4 a, const f32x4 b) { v4u w; w.x = cvt_pk_bf16(a[0], a[1]); w.y = cvt_pk_bf16(a[2], a[3]); w.z = cvt_pk_bf16(b[0], b[1]); w.w = cvt_pk_bf16(b[2], b[3]); return w; }
; __device__ __forceinline__ float fexp(float x) { return __builtin_amdgcn_exp2f(x * 1.4426950408889634f); }
; #define EPI_LOOP_AM for (int ai = 0; ai < 2; ++ai) _Pragma("unroll") for (int m = 0; m < 4; ++m)
;     __device__ __forceinline__ void operator()(AccI& acci, const Unit& u, LAS unsigned char*, int wr, int wc, int fr, int fq) const {
;     ...
;             EPI_LOOP_AM {
;                 const int r = 128 * ai + 64 * wr + 16 * m + fr, tok = pm * 256 + r; const float sxr = sx0[tok];
; #pragma unroll
;                 for (int bj = 0; bj < 2; ++bj) { f32x4 v[2];
; #pragma unroll
;                     for (int n = 0; n < 2; ++n)
; #pragma unroll
;                         for (int j = 0; j < 4; ++j) { const float g = ACCF(ai, bj, m, n, j); v[n][j] = g * __builtin_amdgcn_rcpf(1.f + fexp(-g)); }
;                     *(GAS v4u*)(gs + (size_t)tok * RW + (pn - 8) * 256 + bj * 128 + c0) = pack8(v[0], v[1]); }
	s_nop 0
	v_mul_f32_e32 v159, v156, v159
	v_cvt_f32_i32_e32 v156, v69
	v_mul_f32_e32 v156, v165, v156
	v_mul_f32_e32 v165, 0xbfb8aa3b, v156
	v_exp_f32_e32 v165, v165
	s_nop 0
	v_add_f32_e32 v165, 1.0, v165
	v_rcp_f32_e32 v165, v165
	s_nop 0
	v_mul_f32_e32 v165, v156, v165
	v_cvt_f32_i32_e32 v156, v70
	v_mul_f32_e32 v156, v166, v156
	v_mul_f32_e32 v166, 0xbfb8aa3b, v156
	v_exp_f32_e32 v166, v166
	s_nop 0
	v_add_f32_e32 v166, 1.0, v166
	v_rcp_f32_e32 v166, v166
	s_nop 0
	v_mul_f32_e32 v166, v156, v166
	v_cvt_f32_i32_e32 v156, v71
	v_mul_f32_e32 v156, v167, v156
	v_mul_f32_e32 v167, 0xbfb8aa3b, v156
	v_exp_f32_e32 v167, v167
	s_nop 0
	v_add_f32_e32 v167, 1.0, v167
	v_rcp_f32_e32 v167, v167
	s_nop 0
	v_mul_f32_e32 v167, v156, v167
	v_cvt_pk_bf16_f32 v156, v148, v155
	v_cvt_f32_i32_e32 v148, v72
	v_mul_f32_e32 v155, v44, v145
	v_cvt_pk_bf16_f32 v157, v157, v158
	v_cvt_pk_bf16_f32 v158, v159, v165
	v_mul_f32_e32 v148, v155, v148
	v_mul_f32_e32 v155, 0xbfb8aa3b, v148
	v_exp_f32_e32 v155, v155
	v_cvt_pk_bf16_f32 v159, v166, v167
	global_store_dwordx4 v[152:153], v[156:159], off
	v_mul_f32_e32 v165, v37, v145
	v_add_f32_e32 v155, 1.0, v155
	v_rcp_f32_e32 v155, v155
	v_mul_f32_e32 v156, v45, v145
	v_mul_f32_e32 v157, v46, v145
	v_mul_f32_e32 v158, v47, v145
	v_mul_f32_e32 v148, v148, v155
	v_cvt_f32_i32_e32 v155, v73
	v_mul_f32_e32 v159, v36, v145
	v_mul_f32_e32 v166, v38, v145
	v_mul_f32_e32 v145, v39, v145
	v_mul_f32_e32 v155, v156, v155
	v_mul_f32_e32 v156, 0xbfb8aa3b, v155
	v_exp_f32_e32 v156, v156
	s_nop 0
	v_add_f32_e32 v156, 1.0, v156
	v_rcp_f32_e32 v156, v156
	s_nop 0
	v_mul_f32_e32 v155, v155, v156
	v_cvt_f32_i32_e32 v156, v74
	v_mul_f32_e32 v156, v157, v156
	v_mul_f32_e32 v157, 0xbfb8aa3b, v156
	v_exp_f32_e32 v157, v157
	s_nop 0
	v_add_f32_e32 v157, 1.0, v157
	v_rcp_f32_e32 v157, v157
	s_nop 0
	v_mul_f32_e32 v157, v156, v157
	v_cvt_f32_i32_e32 v156, v75
	v_mul_f32_e32 v156, v158, v156
	v_mul_f32_e32 v158, 0xbfb8aa3b, v156
	v_exp_f32_e32 v158, v158
	s_nop 0
	v_add_f32_e32 v158, 1.0, v158
	v_rcp_f32_e32 v158, v158
	s_nop 0
	v_mul_f32_e32 v158, v156, v158
	v_cvt_f32_i32_e32 v156, v64
	v_mul_f32_e32 v156, v159, v156
	v_mul_f32_e32 v159, 0xbfb8aa3b, v156
	v_exp_f32_e32 v159, v159
	s_nop 0
	v_add_f32_e32 v159, 1.0, v159
	v_rcp_f32_e32 v159, v159
	s_nop 0
	v_mul_f32_e32 v159, v156, v159
	v_cvt_f32_i32_e32 v156, v65
	v_mul_f32_e32 v156, v165, v156
	v_mul_f32_e32 v165, 0xbfb8aa3b, v156
	v_exp_f32_e32 v165, v165
	s_nop 0
	v_add_f32_e32 v165, 1.0, v165
	v_rcp_f32_e32 v165, v165
	s_nop 0
	v_mul_f32_e32 v165, v156, v165
	v_cvt_f32_i32_e32 v156, v66
	v_mul_f32_e32 v156, v166, v156
	v_mul_f32_e32 v166, 0xbfb8aa3b, v156
	v_exp_f32_e32 v166, v166
	s_nop 0
	v_add_f32_e32 v166, 1.0, v166
	v_rcp_f32_e32 v166, v166
	s_nop 0
	v_mul_f32_e32 v166, v156, v166
	v_cvt_f32_i32_e32 v156, v67
	v_mul_f32_e32 v145, v145, v156
	v_mul_f32_e32 v156, 0xbfb8aa3b, v145
	v_exp_f32_e32 v156, v156
	s_nop 0
	v_add_f32_e32 v156, 1.0, v156
	v_rcp_f32_e32 v156, v156
	s_nop 0
	v_mul_f32_e32 v145, v145, v156
	v_cvt_pk_bf16_f32 v156, v148, v155
	v_cvt_pk_bf16_f32 v157, v157, v158
	v_cvt_pk_bf16_f32 v158, v159, v165
	v_cvt_pk_bf16_f32 v159, v166, v145
	global_store_dwordx4 v[152:153], v[156:159], off offset:256
	v_add_u32_e32 v152, 0x90, v144
	v_ashrrev_i32_e32 v153, 31, v152
	v_lshl_add_u64 v[156:157], v[152:153], 2, s[34:35]
	v_mov_b32_e32 v145, v220
	v_cvt_f32_i32_e32 v148, v60
	v_lshlrev_b64 v[152:153], 11, v[152:153]
	v_lshl_add_u64 v[152:153], s[42:43], 0, v[152:153]
	v_lshl_add_u64 v[152:153], v[152:153], 0, s[72:73]
	v_lshl_add_u64 v[152:153], v[152:153], 0, v[146:147]
	v_mul_f32_e32 v155, v40, v145
	v_mul_f32_e32 v148, v155, v148
	v_mul_f32_e32 v155, 0xbfb8aa3b, v148
	v_exp_f32_e32 v155, v155
	v_mul_f32_e32 v156, v41, v145
	v_mul_f32_e32 v157, v42, v145
	v_mul_f32_e32 v158, v43, v145
	v_add_f32_e32 v155, 1.0, v155
	v_rcp_f32_e32 v155, v155
	v_mul_f32_e32 v159, v32, v145
	v_mul_f32_e32 v165, v33, v145
	v_mul_f32_e32 v166, v34, v145
	v_mul_f32_e32 v148, v148, v155
	v_cvt_f32_i32_e32 v155, v61
	v_mul_f32_e32 v167, v35, v145
	v_mul_f32_e32 v155, v156, v155
	v_mul_f32_e32 v156, 0xbfb8aa3b, v155
	v_exp_f32_e32 v156, v156
	s_nop 0
	v_add_f32_e32 v156, 1.0, v156
	v_rcp_f32_e32 v156, v156
	s_nop 0
	v_mul_f32_e32 v155, v155, v156
	v_cvt_f32_i32_e32 v156, v62
	v_mul_f32_e32 v156, v157, v156
	v_mul_f32_e32 v157, 0xbfb8aa3b, v156
	v_exp_f32_e32 v157, v157
	s_nop 0
	v_add_f32_e32 v157, 1.0, v157
	v_rcp_f32_e32 v157, v157
	s_nop 0
	v_mul_f32_e32 v157, v156, v157
	v_cvt_f32_i32_e32 v156, v63
	v_mul_f32_e32 v156, v158, v156
	v_mul_f32_e32 v158, 0xbfb8aa3b, v156
	v_exp_f32_e32 v158, v158
	s_nop 0
	v_add_f32_e32 v158, 1.0, v158
	v_rcp_f32_e32 v158, v158
	s_nop 0
	v_mul_f32_e32 v158, v156, v158
	v_cvt_f32_i32_e32 v156, v52
	v_mul_f32_e32 v156, v159, v156
	v_mul_f32_e32 v159, 0xbfb8aa3b, v156
	v_exp_f32_e32 v159, v159
	s_nop 0
	v_add_f32_e32 v159, 1.0, v159
	v_rcp_f32_e32 v159, v159
	s_nop 0
	v_mul_f32_e32 v159, v156, v159
	v_cvt_f32_i32_e32 v156, v53
	v_mul_f32_e32 v156, v165, v156
	v_mul_f32_e32 v165, 0xbfb8aa3b, v156
	v_exp_f32_e32 v165, v165
	s_nop 0
	v_add_f32_e32 v165, 1.0, v165
	v_rcp_f32_e32 v165, v165
	s_nop 0
	v_mul_f32_e32 v165, v156, v165
	v_cvt_f32_i32_e32 v156, v54
	v_mul_f32_e32 v156, v166, v156
	v_mul_f32_e32 v166, 0xbfb8aa3b, v156
	v_exp_f32_e32 v166, v166
	s_nop 0
	v_add_f32_e32 v166, 1.0, v166
	v_rcp_f32_e32 v166, v166
	s_nop 0
	v_mul_f32_e32 v166, v156, v166
	v_cvt_f32_i32_e32 v156, v55
	v_mul_f32_e32 v156, v167, v156
	v_mul_f32_e32 v167, 0xbfb8aa3b, v156
	v_exp_f32_e32 v167, v167
	s_nop 0
	v_add_f32_e32 v167, 1.0, v167
	v_rcp_f32_e32 v167, v167
	s_nop 0
	v_mul_f32_e32 v167, v156, v167
; #define GAS __attribute__((address_space(1)))
; __device__ __forceinline__ v4u pack8(const f32x4 a, const f32x4 b) { v4u w; w.x = cvt_pk_bf16(a[0], a[1]); w.y = cvt_pk_bf16(a[2], a[3]); w.z = cvt_pk_bf16(b[0], b[1]); w.w = cvt_pk_bf16(b[2], b[3]); return w; }
; __device__ __forceinline__ float fexp(float x) { return __builtin_amdgcn_exp2f(x * 1.4426950408889634f); }
; #define EPI_LOOP_AM for (int ai = 0; ai < 2; ++ai) _Pragma("unroll") for (int m = 0; m < 4; ++m)
;     __device__ __forceinline__ void operator()(AccI& acci, const Unit& u, LAS unsigned char*, int wr, int wc, int fr, int fq) const {
;     ...
;             EPI_LOOP_AM {
;                 const int r = 128 * ai + 64 * wr + 16 * m + fr, tok = pm * 256 + r; const float sxr = sx0[tok];
; #pragma unroll
;                 for (int bj = 0; bj < 2; ++bj) { f32x4 v[2];
; #pragma unroll
;                     for (int n = 0; n < 2; ++n)
; #pragma unroll
;                         for (int j = 0; j < 4; ++j) { const float g = ACCF(ai, bj, m, n, j); v[n][j] = g * __builtin_amdgcn_rcpf(1.f + fexp(-g)); }
;                     *(GAS v4u*)(gs + (size_t)tok * RW + (pn - 8) * 256 + bj * 128 + c0) = pack8(v[0], v[1]); }
	v_cvt_pk_bf16_f32 v156, v148, v155
	v_cvt_f32_i32_e32 v148, v56
	v_mul_f32_e32 v155, v44, v145
	v_cvt_pk_bf16_f32 v157, v157, v158
	v_cvt_pk_bf16_f32 v158, v159, v165
	v_mul_f32_e32 v148, v155, v148
	v_mul_f32_e32 v155, 0xbfb8aa3b, v148
	v_exp_f32_e32 v155, v155
	v_cvt_pk_bf16_f32 v159, v166, v167
	global_store_dwordx4 v[152:153], v[156:159], off
	v_mul_f32_e32 v165, v37, v145
	v_add_f32_e32 v155, 1.0, v155
	v_rcp_f32_e32 v155, v155
	v_mul_f32_e32 v156, v45, v145
	v_mul_f32_e32 v157, v46, v145
	v_mul_f32_e32 v158, v47, v145
	v_mul_f32_e32 v148, v148, v155
	v_cvt_f32_i32_e32 v155, v57
	v_mul_f32_e32 v159, v36, v145
	v_mul_f32_e32 v166, v38, v145
	v_mul_f32_e32 v145, v39, v145
	v_mul_f32_e32 v155, v156, v155
	v_mul_f32_e32 v156, 0xbfb8aa3b, v155
	v_exp_f32_e32 v156, v156
	s_nop 0
	v_add_f32_e32 v156, 1.0, v156
	v_rcp_f32_e32 v156, v156
	s_nop 0
	v_mul_f32_e32 v155, v155, v156
	v_cvt_f32_i32_e32 v156, v58
	v_mul_f32_e32 v156, v157, v156
	v_mul_f32_e32 v157, 0xbfb8aa3b, v156
	v_exp_f32_e32 v157, v157
	s_nop 0
	v_add_f32_e32 v157, 1.0, v157
	v_rcp_f32_e32 v157, v157
	s_nop 0
	v_mul_f32_e32 v157, v156, v157
	v_cvt_f32_i32_e32 v156, v59
	v_mul_f32_e32 v156, v158, v156
	v_mul_f32_e32 v158, 0xbfb8aa3b, v156
	v_exp_f32_e32 v158, v158
	s_nop 0
	v_add_f32_e32 v158, 1.0, v158
	v_rcp_f32_e32 v158, v158
	s_nop 0
	v_mul_f32_e32 v158, v156, v158
	v_cvt_f32_i32_e32 v156, v48
	v_mul_f32_e32 v156, v159, v156
	v_mul_f32_e32 v159, 0xbfb8aa3b, v156
	v_exp_f32_e32 v159, v159
	s_nop 0
	v_add_f32_e32 v159, 1.0, v159
	v_rcp_f32_e32 v159, v159
	s_nop 0
	v_mul_f32_e32 v159, v156, v159
	v_cvt_f32_i32_e32 v156, v49
	v_mul_f32_e32 v156, v165, v156
	v_mul_f32_e32 v165, 0xbfb8aa3b, v156
	v_exp_f32_e32 v165, v165
	s_nop 0
	v_add_f32_e32 v165, 1.0, v165
	v_rcp_f32_e32 v165, v165
	s_nop 0
	v_mul_f32_e32 v165, v156, v165
	v_cvt_f32_i32_e32 v156, v50
	v_mul_f32_e32 v156, v166, v156
	v_mul_f32_e32 v166, 0xbfb8aa3b, v156
	v_exp_f32_e32 v166, v166
	s_nop 0
	v_add_f32_e32 v166, 1.0, v166
	v_rcp_f32_e32 v166, v166
	s_nop 0
	v_mul_f32_e32 v166, v156, v166
	v_cvt_f32_i32_e32 v156, v51
	v_mul_f32_e32 v145, v145, v156
	v_mul_f32_e32 v156, 0xbfb8aa3b, v145
	v_exp_f32_e32 v156, v156
	s_nop 0
	v_add_f32_e32 v156, 1.0, v156
	v_rcp_f32_e32 v156, v156
	s_nop 0
	v_mul_f32_e32 v145, v145, v156
	v_cvt_pk_bf16_f32 v156, v148, v155
	v_cvt_pk_bf16_f32 v157, v157, v158
	v_cvt_pk_bf16_f32 v158, v159, v165
	v_cvt_pk_bf16_f32 v159, v166, v145
	global_store_dwordx4 v[152:153], v[156:159], off offset:256
	v_add_u32_e32 v152, 0xa0, v144
	v_ashrrev_i32_e32 v153, 31, v152
	v_lshl_add_u64 v[156:157], v[152:153], 2, s[34:35]
	v_mov_b32_e32 v145, v221
	v_cvt_f32_i32_e32 v148, v28
	v_lshlrev_b64 v[152:153], 11, v[152:153]
	v_lshl_add_u64 v[152:153], s[42:43], 0, v[152:153]
	v_lshl_add_u64 v[152:153], v[152:153], 0, s[72:73]
	v_lshl_add_u64 v[152:153], v[152:153], 0, v[146:147]
	v_add_u32_e32 v144, 0xb0, v144
	v_mul_f32_e32 v155, v40, v145
	v_mul_f32_e32 v148, v155, v148
	v_mul_f32_e32 v155, 0xbfb8aa3b, v148
	v_exp_f32_e32 v155, v155
	v_mul_f32_e32 v156, v41, v145
	v_mul_f32_e32 v157, v42, v145
	v_mul_f32_e32 v158, v43, v145
	v_add_f32_e32 v155, 1.0, v155
	v_rcp_f32_e32 v155, v155
	v_mul_f32_e32 v159, v32, v145
	v_mul_f32_e32 v165, v33, v145
	v_mul_f32_e32 v166, v34, v145
	v_mul_f32_e32 v148, v148, v155
	v_cvt_f32_i32_e32 v155, v29
	v_mul_f32_e32 v167, v35, v145
	v_mul_f32_e32 v155, v156, v155
	v_mul_f32_e32 v156, 0xbfb8aa3b, v155
	v_exp_f32_e32 v156, v156
	s_nop 0
	v_add_f32_e32 v156, 1.0, v156
	v_rcp_f32_e32 v156, v156
	s_nop 0
	v_mul_f32_e32 v155, v155, v156
	v_cvt_f32_i32_e32 v156, v30
	v_mul_f32_e32 v156, v157, v156
	v_mul_f32_e32 v157, 0xbfb8aa3b, v156
	v_exp_f32_e32 v157, v157
	s_nop 0
	v_add_f32_e32 v157, 1.0, v157
	v_rcp_f32_e32 v157, v157
	s_nop 0
	v_mul_f32_e32 v157, v156, v157
	v_cvt_f32_i32_e32 v156, v31
	v_mul_f32_e32 v156, v158, v156
	v_mul_f32_e32 v158, 0xbfb8aa3b, v156
	v_exp_f32_e32 v158, v158
	s_nop 0
	v_add_f32_e32 v158, 1.0, v158
	v_rcp_f32_e32 v158, v158
	s_nop 0
	v_mul_f32_e32 v158, v156, v158
	v_cvt_f32_i32_e32 v156, v20
	v_mul_f32_e32 v156, v159, v156
	v_mul_f32_e32 v159, 0xbfb8aa3b, v156
	v_exp_f32_e32 v159, v159
	s_nop 0
	v_add_f32_e32 v159, 1.0, v159
	v_rcp_f32_e32 v159, v159
	s_nop 0
	v_mul_f32_e32 v159, v156, v159
	v_cvt_f32_i32_e32 v156, v21
	v_mul_f32_e32 v156, v165, v156
	v_mul_f32_e32 v165, 0xbfb8aa3b, v156
	v_exp_f32_e32 v165, v165
	s_nop 0
	v_add_f32_e32 v165, 1.0, v165
	v_rcp_f32_e32 v165, v165
	s_nop 0
	v_mul_f32_e32 v165, v156, v165
	v_cvt_f32_i32_e32 v156, v22
	v_mul_f32_e32 v156, v166, v156
	v_mul_f32_e32 v166, 0xbfb8aa3b, v156
	v_exp_f32_e32 v166, v166
	s_nop 0
	v_add_f32_e32 v166, 1.0, v166
	v_rcp_f32_e32 v166, v166
	s_nop 0
	v_mul_f32_e32 v166, v156, v166
	v_cvt_f32_i32_e32 v156, v23
	v_mul_f32_e32 v156, v167, v156
	v_mul_f32_e32 v167, 0xbfb8aa3b, v156
	v_exp_f32_e32 v167, v167
	s_nop 0
	v_add_f32_e32 v167, 1.0, v167
	v_rcp_f32_e32 v167, v167
	s_nop 0
	v_mul_f32_e32 v167, v156, v167
	v_cvt_pk_bf16_f32 v156, v148, v155
	v_cvt_f32_i32_e32 v148, v24
	v_mul_f32_e32 v155, v44, v145
	v_cvt_pk_bf16_f32 v157, v157, v158
	v_cvt_pk_bf16_f32 v158, v159, v165
	v_mul_f32_e32 v148, v155, v148
	v_mul_f32_e32 v155, 0xbfb8aa3b, v148
	v_exp_f32_e32 v155, v155
	v_cvt_pk_bf16_f32 v159, v166, v167
	global_store_dwordx4 v[152:153], v[156:159], off
	v_mul_f32_e32 v165, v37, v145
	v_add_f32_e32 v155, 1.0, v155
	v_rcp_f32_e32 v155, v155
	v_mul_f32_e32 v156, v45, v145
	v_mul_f32_e32 v157, v46, v145
	v_mul_f32_e32 v158, v47, v145
	v_mul_f32_e32 v148, v148, v155
	v_cvt_f32_i32_e32 v155, v25
	v_mul_f32_e32 v159, v36, v145
	v_mul_f32_e32 v166, v38, v145
	v_mul_f32_e32 v145, v39, v145
; #define GAS __attribute__((address_space(1)))
; __device__ __forceinline__ v4u pack8(const f32x4 a, const f32x4 b) { v4u w; w.x = cvt_pk_bf16(a[0], a[1]); w.y = cvt_pk_bf16(a[2], a[3]); w.z = cvt_pk_bf16(b[0], b[1]); w.w = cvt_pk_bf16(b[2], b[3]); return w; }
; __device__ __forceinline__ float fexp(float x) { return __builtin_amdgcn_exp2f(x * 1.4426950408889634f); }
; #define EPI_LOOP_AM for (int ai = 0; ai < 2; ++ai) _Pragma("unroll") for (int m = 0; m < 4; ++m)
;     __device__ __forceinline__ void operator()(AccI& acci, const Unit& u, LAS unsigned char*, int wr, int wc, int fr, int fq) const {
;     ...
;             EPI_LOOP_AM {
;                 const int r = 128 * ai + 64 * wr + 16 * m + fr, tok = pm * 256 + r; const float sxr = sx0[tok];
; #pragma unroll
;                 for (int bj = 0; bj < 2; ++bj) { f32x4 v[2];
; #pragma unroll
;                     for (int n = 0; n < 2; ++n)
; #pragma unroll
;                         for (int j = 0; j < 4; ++j) { const float g = ACCF(ai, bj, m, n, j); v[n][j] = g * __builtin_amdgcn_rcpf(1.f + fexp(-g)); }
;                     *(GAS v4u*)(gs + (size_t)tok * RW + (pn - 8) * 256 + bj * 128 + c0) = pack8(v[0], v[1]); }
	v_mul_f32_e32 v155, v156, v155
	v_mul_f32_e32 v156, 0xbfb8aa3b, v155
	v_exp_f32_e32 v156, v156
	s_nop 0
	v_add_f32_e32 v156, 1.0, v156
	v_rcp_f32_e32 v156, v156
	s_nop 0
	v_mul_f32_e32 v155, v155, v156
	v_cvt_f32_i32_e32 v156, v26
	v_mul_f32_e32 v156, v157, v156
	v_mul_f32_e32 v157, 0xbfb8aa3b, v156
	v_exp_f32_e32 v157, v157
	s_nop 0
	v_add_f32_e32 v157, 1.0, v157
	v_rcp_f32_e32 v157, v157
	s_nop 0
	v_mul_f32_e32 v157, v156, v157
	v_cvt_f32_i32_e32 v156, v27
	v_mul_f32_e32 v156, v158, v156
	v_mul_f32_e32 v158, 0xbfb8aa3b, v156
	v_exp_f32_e32 v158, v158
	s_nop 0
	v_add_f32_e32 v158, 1.0, v158
	v_rcp_f32_e32 v158, v158
	s_nop 0
	v_mul_f32_e32 v158, v156, v158
	v_cvt_f32_i32_e32 v156, v16
	v_mul_f32_e32 v156, v159, v156
	v_mul_f32_e32 v159, 0xbfb8aa3b, v156
	v_exp_f32_e32 v159, v159
	s_nop 0
	v_add_f32_e32 v159, 1.0, v159
	v_rcp_f32_e32 v159, v159
	s_nop 0
	v_mul_f32_e32 v159, v156, v159
	v_cvt_f32_i32_e32 v156, v17
	v_mul_f32_e32 v156, v165, v156
	v_mul_f32_e32 v165, 0xbfb8aa3b, v156
	v_exp_f32_e32 v165, v165
	s_nop 0
	v_add_f32_e32 v165, 1.0, v165
	v_rcp_f32_e32 v165, v165
	s_nop 0
	v_mul_f32_e32 v165, v156, v165
	v_cvt_f32_i32_e32 v156, v18
	v_mul_f32_e32 v156, v166, v156
	v_mul_f32_e32 v166, 0xbfb8aa3b, v156
	v_exp_f32_e32 v166, v166
	s_nop 0
	v_add_f32_e32 v166, 1.0, v166
	v_rcp_f32_e32 v166, v166
	s_nop 0
	v_mul_f32_e32 v166, v156, v166
	v_cvt_f32_i32_e32 v156, v19
	v_mul_f32_e32 v145, v145, v156
	v_mul_f32_e32 v156, 0xbfb8aa3b, v145
	v_exp_f32_e32 v156, v156
	s_nop 0
	v_add_f32_e32 v156, 1.0, v156
	v_rcp_f32_e32 v156, v156
	s_nop 0
	v_mul_f32_e32 v145, v145, v156
	v_cvt_pk_bf16_f32 v156, v148, v155
	v_cvt_pk_bf16_f32 v157, v157, v158
	v_cvt_pk_bf16_f32 v158, v159, v165
	v_cvt_pk_bf16_f32 v159, v166, v145
	v_ashrrev_i32_e32 v145, 31, v144
	global_store_dwordx4 v[152:153], v[156:159], off offset:256
	v_lshl_add_u64 v[152:153], v[144:145], 2, s[34:35]
	v_mov_b32_e32 v148, v222
	v_cvt_f32_i32_e32 v152, v12
	v_lshlrev_b64 v[144:145], 11, v[144:145]
	v_lshl_add_u64 v[144:145], s[42:43], 0, v[144:145]
	v_lshl_add_u64 v[144:145], v[144:145], 0, s[72:73]
	s_mov_b64 s[72:73], 0
	v_mul_f32_e32 v153, v40, v148
	v_mul_f32_e32 v152, v153, v152
	v_mul_f32_e32 v153, 0xbfb8aa3b, v152
	v_exp_f32_e32 v153, v153
	v_mul_f32_e32 v155, v41, v148
	v_mul_f32_e32 v156, v42, v148
	v_mul_f32_e32 v157, v43, v148
	v_add_f32_e32 v153, 1.0, v153
	v_rcp_f32_e32 v153, v153
	v_mul_f32_e32 v158, v32, v148
	v_mul_f32_e32 v159, v33, v148
	v_mul_f32_e32 v165, v34, v148
	v_mul_f32_e32 v152, v152, v153
	v_cvt_f32_i32_e32 v153, v13
	v_mul_f32_e32 v166, v35, v148
	v_mul_f32_e32 v153, v155, v153
	v_mul_f32_e32 v155, 0xbfb8aa3b, v153
	v_exp_f32_e32 v155, v155
	s_nop 0
	v_add_f32_e32 v155, 1.0, v155
	v_rcp_f32_e32 v155, v155
	s_nop 0
	v_mul_f32_e32 v153, v153, v155
	v_cvt_f32_i32_e32 v155, v14
	v_mul_f32_e32 v155, v156, v155
	v_mul_f32_e32 v156, 0xbfb8aa3b, v155
	v_exp_f32_e32 v156, v156
	s_nop 0
	v_add_f32_e32 v156, 1.0, v156
	v_rcp_f32_e32 v156, v156
	s_nop 0
	v_mul_f32_e32 v155, v155, v156
	v_cvt_f32_i32_e32 v156, v15
	v_mul_f32_e32 v156, v157, v156
	v_mul_f32_e32 v157, 0xbfb8aa3b, v156
	v_exp_f32_e32 v157, v157
	s_nop 0
	v_add_f32_e32 v157, 1.0, v157
	v_rcp_f32_e32 v157, v157
	s_nop 0
	v_mul_f32_e32 v157, v156, v157
	v_cvt_f32_i32_e32 v156, v4
	v_mul_f32_e32 v156, v158, v156
	v_mul_f32_e32 v158, 0xbfb8aa3b, v156
	v_exp_f32_e32 v158, v158
	s_nop 0
	v_add_f32_e32 v158, 1.0, v158
	v_rcp_f32_e32 v158, v158
	s_nop 0
	v_mul_f32_e32 v158, v156, v158
	v_cvt_f32_i32_e32 v156, v5
	v_mul_f32_e32 v156, v159, v156
	v_mul_f32_e32 v159, 0xbfb8aa3b, v156
	v_exp_f32_e32 v159, v159
	s_nop 0
	v_add_f32_e32 v159, 1.0, v159
	v_rcp_f32_e32 v159, v159
	s_nop 0
	v_mul_f32_e32 v159, v156, v159
	v_cvt_f32_i32_e32 v156, v6
	v_mul_f32_e32 v156, v165, v156
	v_mul_f32_e32 v165, 0xbfb8aa3b, v156
	v_exp_f32_e32 v165, v165
	s_nop 0
	v_add_f32_e32 v165, 1.0, v165
	v_rcp_f32_e32 v165, v165
	s_nop 0
	v_mul_f32_e32 v165, v156, v165
	v_cvt_f32_i32_e32 v156, v7
	v_mul_f32_e32 v156, v166, v156
	v_mul_f32_e32 v166, 0xbfb8aa3b, v156
	v_exp_f32_e32 v166, v166
	s_nop 0
	v_add_f32_e32 v166, 1.0, v166
	v_rcp_f32_e32 v166, v166
	s_nop 0
	v_mul_f32_e32 v166, v156, v166
	v_cvt_pk_bf16_f32 v156, v152, v153
	v_lshl_add_u64 v[152:153], v[144:145], 0, v[146:147]
	v_cvt_f32_i32_e32 v144, v8
	v_mul_f32_e32 v145, v44, v148
	v_mul_f32_e32 v146, v45, v148
	v_mul_f32_e32 v147, v46, v148
	v_mul_f32_e32 v144, v145, v144
	v_mul_f32_e32 v145, 0xbfb8aa3b, v144
	v_exp_f32_e32 v145, v145
	v_cvt_pk_bf16_f32 v157, v155, v157
	v_mul_f32_e32 v155, v47, v148
	v_cvt_pk_bf16_f32 v158, v158, v159
	v_add_f32_e32 v145, 1.0, v145
	v_rcp_f32_e32 v145, v145
	v_cvt_pk_bf16_f32 v159, v165, v166
	global_store_dwordx4 v[152:153], v[156:159], off
	v_lshl_add_u64 v[152:153], v[152:153], 0, s[52:53]
	v_mul_f32_e32 v144, v144, v145
	v_cvt_f32_i32_e32 v145, v9
	v_mul_f32_e32 v156, v36, v148
	v_mul_f32_e32 v157, v37, v148
	v_mul_f32_e32 v158, v38, v148
	v_mul_f32_e32 v145, v146, v145
	v_mul_f32_e32 v146, 0xbfb8aa3b, v145
	v_exp_f32_e32 v146, v146
	v_mul_f32_e32 v148, v39, v148
	v_add_f32_e32 v146, 1.0, v146
	v_rcp_f32_e32 v146, v146
	s_nop 0
	v_mul_f32_e32 v145, v145, v146
	v_cvt_f32_i32_e32 v146, v10
	v_cvt_pk_bf16_f32 v144, v144, v145
	v_mul_f32_e32 v146, v147, v146
	v_mul_f32_e32 v147, 0xbfb8aa3b, v146
	v_exp_f32_e32 v147, v147
	s_nop 0
	v_add_f32_e32 v147, 1.0, v147
	v_rcp_f32_e32 v147, v147
	s_nop 0
	v_mul_f32_e32 v146, v146, v147
	v_cvt_f32_i32_e32 v147, v11
	v_mul_f32_e32 v147, v155, v147
	v_mul_f32_e32 v155, 0xbfb8aa3b, v147
	v_exp_f32_e32 v155, v155
	s_nop 0
	v_add_f32_e32 v155, 1.0, v155
	v_rcp_f32_e32 v155, v155
	s_nop 0
	v_mul_f32_e32 v147, v147, v155
	v_cvt_f32_i32_e32 v155, v0
	v_cvt_pk_bf16_f32 v145, v146, v147
	v_mul_f32_e32 v155, v156, v155
	v_mul_f32_e32 v156, 0xbfb8aa3b, v155
	v_exp_f32_e32 v156, v156
	s_nop 0
	v_add_f32_e32 v156, 1.0, v156
	v_rcp_f32_e32 v156, v156
	s_nop 0
	v_mul_f32_e32 v155, v155, v156
	v_cvt_f32_i32_e32 v156, v1
	v_mul_f32_e32 v156, v157, v156
	v_mul_f32_e32 v157, 0xbfb8aa3b, v156
	v_exp_f32_e32 v157, v157
	s_nop 0
	v_add_f32_e32 v157, 1.0, v157
	v_rcp_f32_e32 v157, v157
	s_nop 0
	v_mul_f32_e32 v156, v156, v157
	v_cvt_f32_i32_e32 v157, v2
	v_cvt_pk_bf16_f32 v146, v155, v156
	v_mul_f32_e32 v157, v158, v157
	v_mul_f32_e32 v158, 0xbfb8aa3b, v157
	v_exp_f32_e32 v158, v158
	s_nop 0
	v_add_f32_e32 v158, 1.0, v158
	v_rcp_f32_e32 v158, v158
	s_nop 0
	v_mul_f32_e32 v157, v157, v158
	v_cvt_f32_i32_e32 v158, v3
	v_mul_f32_e32 v148, v148, v158
	v_mul_f32_e32 v158, 0xbfb8aa3b, v148
	v_exp_f32_e32 v158, v158
	s_nop 0
	v_add_f32_e32 v158, 1.0, v158
	v_rcp_f32_e32 v158, v158
	s_nop 0
	v_mul_f32_e32 v148, v148, v158
	v_cvt_pk_bf16_f32 v147, v157, v148
; #define GAS __attribute__((address_space(1)))
; __device__ __forceinline__ v4u pack8(const f32x4 a, const f32x4 b) { v4u w; w.x = cvt_pk_bf16(a[0], a[1]); w.y = cvt_pk_bf16(a[2], a[3]); w.z = cvt_pk_bf16(b[0], b[1]); w.w = cvt_pk_bf16(b[2], b[3]); return w; }
; __device__ __forceinline__ float fexp(float x) { return __builtin_amdgcn_exp2f(x * 1.4426950408889634f); }
; #define EPI_LOOP_AM for (int ai = 0; ai < 2; ++ai) _Pragma("unroll") for (int m = 0; m < 4; ++m)
;     __device__ __forceinline__ void operator()(AccI& acci, const Unit& u, LAS unsigned char*, int wr, int wc, int fr, int fq) const {
;     ...
;         if (pn < 8) {
;             const int h = pn & 3; const bool isq = pn < 4;
;             float inv[8];
; #pragma unroll
;             for (int e = 0; e < 8; ++e) inv[e] = __builtin_amdgcn_exp2f(-(float)(c0 + e) * (13.287712379549449f / 128.f)) * 0.15915494309189535f;
;             const float lgf = -fexp(dec_f[h]), lgb = -fexp(dec_b[h]);
; #pragma unroll
;             EPI_LOOP_AM {
;                 const int r = 128 * ai + 64 * wr + 16 * m + fr, tok = pm * 256 + r; const float pos = (float)tok; const float sxr = sx0[tok];
;                 f32x4 o1[2], o2[2];
; #pragma unroll
;                 for (int n = 0; n < 2; ++n)
; #pragma unroll
;                     for (int j = 0; j < 4; ++j) { float c, s; cs_rev(pos * inv[4 * n + j], c, s); const float x1 = ACCF(ai, 0, m, n, j), x2 = ACCF(ai, 1, m, n, j); o1[n][j] = x1 * c - x2 * s; o2[n][j] = x2 * c + x1 * s; }
;                 if (isq) {
;                     bf16* q = qs + (size_t)tok * RW + h * HD + c0; *(GAS v4u*)q = pack8(o1[0], o1[1]); *(GAS v4u*)(q + 128) = pack8(o2[0], o2[1]);
;                     const int il = r; const float wf = fexp(lgf * (float)(il + 1)), wb = fexp(lgb * (float)(255 - il));
;                     bf16* a = Acat + ((size_t)h * T + tok) * CAT + c0;
;                     *(GAS v4u*)(a + 256) = pack8(o1[0] * wf, o1[1] * wf); *(GAS v4u*)(a + 384) = pack8(o2[0] * wf, o2[1] * wf);
;                     *(GAS v4u*)(a + 512) = pack8(o1[0] * wb, o1[1] * wb); *(GAS v4u*)(a + 640) = pack8(o2[0] * wb, o2[1] * wb);
;                 } else {
;                     bf16* k = kk + (size_t)tok * RW + h * HD + c0; *(GAS v4u*)k = pack8(o1[0] * 0.0625f, o1[1] * 0.0625f); *(GAS v4u*)(k + 128) = pack8(o2[0] * 0.0625f, o2[1] * 0.0625f);
.LBB0_184:
	s_andn2_b64 vcc, exec, s[72:73]
	s_cbranch_vccnz .LBB0_217
	v_cvt_f32_i32_e32 v144, v150
	s_and_b32 s0, s24, 3
	s_cmp_gt_i32 s24, 3
	s_cselect_b64 s[72:73], -1, 0
	v_mul_f32_e32 v144, 0xbdd49a78, v144
	v_exp_f32_e32 v144, v144
	s_lshl_b32 s2, s0, 2
	v_add_u32_e32 v172, s26, v154
	v_cvt_f32_i32_e32 v141, v141
	v_mul_f32_e32 v148, 0.15915494, v144
	v_or_b32_e32 v144, 1, v150
	v_cvt_f32_i32_e32 v144, v144
	v_cvt_f32_i32_e32 v140, v140
	v_cvt_f32_i32_e32 v137, v137
	v_cvt_f32_i32_e32 v136, v136
	v_mul_f32_e32 v144, 0xbdd49a78, v144
	v_exp_f32_e32 v144, v144
	v_cvt_f32_i32_e32 v143, v143
	v_cvt_f32_i32_e32 v142, v142
	v_cvt_f32_i32_e32 v139, v139
	v_mul_f32_e32 v165, 0.15915494, v144
	v_or_b32_e32 v144, 2, v150
	v_cvt_f32_i32_e32 v144, v144
	v_cvt_f32_i32_e32 v138, v138
	v_cvt_f32_i32_e32 v133, v133
	v_cvt_f32_i32_e32 v132, v132
	v_mul_f32_e32 v144, 0xbdd49a78, v144
	v_exp_f32_e32 v144, v144
	v_cvt_f32_i32_e32 v129, v129
	v_cvt_f32_i32_e32 v128, v128
	v_cvt_f32_i32_e32 v135, v135
	v_mul_f32_e32 v166, 0.15915494, v144
	v_or_b32_e32 v144, 3, v150
	v_cvt_f32_i32_e32 v144, v144
	v_cvt_f32_i32_e32 v134, v134
	v_cvt_f32_i32_e32 v131, v131
	v_cvt_f32_i32_e32 v130, v130
	v_mul_f32_e32 v144, 0xbdd49a78, v144
	v_exp_f32_e32 v144, v144
	s_lshl_b32 s19, s0, 8
	s_and_b64 vcc, exec, s[72:73]
	v_mul_f32_e32 v167, 0.15915494, v144
	v_or_b32_e32 v144, 4, v150
	v_cvt_f32_i32_e32 v144, v144
	v_mul_f32_e32 v144, 0xbdd49a78, v144
	v_exp_f32_e32 v144, v144
	s_nop 0
	v_mul_f32_e32 v168, 0.15915494, v144
	v_or_b32_e32 v144, 5, v150
	v_cvt_f32_i32_e32 v144, v144
	v_mul_f32_e32 v144, 0xbdd49a78, v144
	v_exp_f32_e32 v144, v144
	s_nop 0
	v_mul_f32_e32 v169, 0.15915494, v144
	v_or_b32_e32 v144, 6, v150
	v_cvt_f32_i32_e32 v144, v144
	v_mul_f32_e32 v144, 0xbdd49a78, v144
	v_exp_f32_e32 v144, v144
	s_nop 0
	v_mul_f32_e32 v170, 0.15915494, v144
	v_or_b32_e32 v144, 7, v150
	v_cvt_f32_i32_e32 v144, v144
	v_mul_f32_e32 v144, 0xbdd49a78, v144
	v_exp_f32_e32 v144, v144
	s_nop 0
	v_mul_f32_e32 v171, 0.15915494, v144
	v_mov_b32_e32 v144, s2
	global_load_dword v174, v144, s[14:15]
	global_load_dword v173, v144, s[30:31]
	v_lshl_add_u32 v144, s4, 8, v172
	v_ashrrev_i32_e32 v145, 31, v144
	v_lshl_add_u64 v[152:153], v[144:145], 2, s[34:35]
	global_load_dword v146, v[152:153], off
	global_load_dword v216, v[152:153], off offset:64
	global_load_dword v217, v[152:153], off offset:128
	global_load_dword v218, v[152:153], off offset:192
	global_load_dword v219, v[152:153], off offset:512
	global_load_dword v220, v[152:153], off offset:576
	global_load_dword v221, v[152:153], off offset:640
	global_load_dword v222, v[152:153], off offset:704
	v_cvt_f32_i32_e32 v147, v144
	s_mov_b64 s[4:5], -1
	v_mul_f32_e32 v152, v148, v147
	v_fract_f32_e32 v153, v152
	v_cos_f32_e32 v152, v153
	v_sin_f32_e32 v154, v153
	v_mul_f32_e32 v153, v165, v147
	v_fract_f32_e32 v155, v153
	v_cos_f32_e32 v153, v155
	v_sin_f32_e32 v155, v155
	s_waitcnt vmcnt(0)
	v_pk_mul_f32 v[156:157], v[40:41], v[146:147] op_sel_hi:[1,0]
	s_nop 0
	v_pk_mul_f32 v[156:157], v[156:157], v[140:141]
	v_pk_mul_f32 v[140:141], v[44:45], v[146:147] op_sel_hi:[1,0]
	s_nop 0
	v_pk_mul_f32 v[136:137], v[140:141], v[136:137]
	s_nop 0
	v_pk_mul_f32 v[140:141], v[154:155], v[136:137]
	v_pk_mul_f32 v[136:137], v[152:153], v[136:137]
	v_pk_fma_f32 v[140:141], v[152:153], v[156:157], v[140:141] neg_lo:[0,0,1] neg_hi:[0,0,1]
	v_mul_f32_e32 v152, v166, v147
	v_mul_f32_e32 v153, v167, v147
	v_fract_f32_e32 v152, v152
	v_fract_f32_e32 v153, v153
	v_pk_fma_f32 v[136:137], v[154:155], v[156:157], v[136:137]
	v_cos_f32_e32 v154, v152
	v_sin_f32_e32 v152, v152
	v_cos_f32_e32 v155, v153
	v_sin_f32_e32 v153, v153
	v_pk_mul_f32 v[156:157], v[42:43], v[146:147] op_sel_hi:[1,0]
	s_nop 0
	v_pk_mul_f32 v[156:157], v[156:157], v[142:143]
	v_pk_mul_f32 v[142:143], v[46:47], v[146:147] op_sel_hi:[1,0]
	s_nop 0
	v_pk_mul_f32 v[138:139], v[142:143], v[138:139]
	s_nop 0
	v_pk_mul_f32 v[142:143], v[152:153], v[138:139]
	v_pk_mul_f32 v[138:139], v[154:155], v[138:139]
	v_pk_fma_f32 v[142:143], v[154:155], v[156:157], v[142:143] neg_lo:[0,0,1] neg_hi:[0,0,1]
	v_pk_fma_f32 v[138:139], v[152:153], v[156:157], v[138:139]
	v_mul_f32_e32 v152, v168, v147
	v_fract_f32_e32 v153, v152
	v_cos_f32_e32 v152, v153
	v_sin_f32_e32 v156, v153
	v_mul_f32_e32 v153, v169, v147
	v_fract_f32_e32 v154, v153
	v_cos_f32_e32 v153, v154
	v_sin_f32_e32 v157, v154
	v_pk_mul_f32 v[154:155], v[32:33], v[146:147] op_sel_hi:[1,0]
	s_nop 0
	v_pk_mul_f32 v[132:133], v[154:155], v[132:133]
	v_pk_mul_f32 v[154:155], v[36:37], v[146:147] op_sel_hi:[1,0]
	s_nop 0
	v_pk_mul_f32 v[128:129], v[154:155], v[128:129]
	s_nop 0
	v_pk_mul_f32 v[154:155], v[156:157], v[128:129]
	v_pk_mul_f32 v[128:129], v[152:153], v[128:129]
	v_pk_fma_f32 v[154:155], v[152:153], v[132:133], v[154:155] neg_lo:[0,0,1] neg_hi:[0,0,1]
	v_pk_fma_f32 v[152:153], v[156:157], v[132:133], v[128:129]
	v_mul_f32_e32 v128, v170, v147
	v_fract_f32_e32 v129, v128
	v_cos_f32_e32 v128, v129
	v_sin_f32_e32 v132, v129
	v_mul_f32_e32 v129, v171, v147
	v_fract_f32_e32 v133, v129
	v_cos_f32_e32 v129, v133
	v_sin_f32_e32 v133, v133
	v_pk_mul_f32 v[156:157], v[34:35], v[146:147] op_sel_hi:[1,0]
	s_nop 0
	v_pk_mul_f32 v[156:157], v[156:157], v[134:135]
	v_pk_mul_f32 v[134:135], v[38:39], v[146:147] op_sel_hi:[1,0]
	s_nop 0
	v_pk_mul_f32 v[130:131], v[134:135], v[130:131]
	s_nop 0
	v_pk_mul_f32 v[134:135], v[128:129], v[130:131]
	v_pk_mul_f32 v[130:131], v[132:133], v[130:131]
	v_pk_fma_f32 v[134:135], v[132:133], v[156:157], v[134:135]
	v_pk_fma_f32 v[146:147], v[128:129], v[156:157], v[130:131] neg_lo:[0,0,1] neg_hi:[0,0,1]
	v_lshlrev_b64 v[156:157], 11, v[144:145]
	s_cbranch_vccz .LBB0_187
	v_lshl_add_u64 v[128:129], s[40:41], 0, v[156:157]
	s_lshl_b32 s6, s19, 1
	v_lshl_add_u64 v[128:129], v[128:129], 0, s[6:7]
	v_lshl_add_u64 v[132:133], v[150:151], 1, v[128:129]
	v_pk_mul_f32 v[130:131], v[142:143], s[54:55] op_sel_hi:[1,0]
	v_pk_mul_f32 v[128:129], v[140:141], s[54:55] op_sel_hi:[1,0]
	v_pk_mul_f32 v[158:159], v[154:155], s[54:55] op_sel_hi:[1,0]
	v_pk_mul_f32 v[176:177], v[146:147], s[54:55] op_sel_hi:[1,0]
	v_cvt_pk_bf16_f32 v128, v128, v129
	v_cvt_pk_bf16_f32 v129, v130, v131
	v_cvt_pk_bf16_f32 v130, v158, v159
	v_pk_mul_f32 v[158:159], v[152:153], s[54:55] op_sel_hi:[1,0]
	v_cvt_pk_bf16_f32 v131, v176, v177
	global_store_dwordx4 v[132:133], v[128:131], off
	v_pk_mul_f32 v[176:177], v[134:135], s[54:55] op_sel_hi:[1,0]
	s_mov_b64 s[4:5], 0
	v_pk_mul_f32 v[130:131], v[138:139], s[54:55] op_sel_hi:[1,0]
	v_pk_mul_f32 v[128:129], v[136:137], s[54:55] op_sel_hi:[1,0]
	s_nop 0
	v_cvt_pk_bf16_f32 v128, v128, v129
	v_cvt_pk_bf16_f32 v129, v130, v131
	v_cvt_pk_bf16_f32 v130, v158, v159
	v_cvt_pk_bf16_f32 v131, v176, v177
	v_lshl_add_u64 v[158:159], v[132:133], 0, s[52:53]

; #define GAS __attribute__((address_space(1)))
; __device__ __forceinline__ v4u pack8(const f32x4 a, const f32x4 b) { v4u w; w.x = cvt_pk_bf16(a[0], a[1]); w.y = cvt_pk_bf16(a[2], a[3]); w.z = cvt_pk_bf16(b[0], b[1]); w.w = cvt_pk_bf16(b[2], b[3]); return w; }
; __device__ __forceinline__ float fexp(float x) { return __builtin_amdgcn_exp2f(x * 1.4426950408889634f); }
; __device__ __forceinline__ void cs_rev(float rev, float& c, float& s) { const float f = __builtin_amdgcn_fractf(rev); c = __builtin_amdgcn_cosf(f); s = __builtin_amdgcn_sinf(f); }
; #define EPI_LOOP_AM for (int ai = 0; ai < 2; ++ai) _Pragma("unroll") for (int m = 0; m < 4; ++m)
;     __device__ __forceinline__ void operator()(AccI& acci, const Unit& u, LAS unsigned char*, int wr, int wc, int fr, int fq) const {
;     ...
;             EPI_LOOP_AM {
;                 const int r = 128 * ai + 64 * wr + 16 * m + fr, tok = pm * 256 + r; const float pos = (float)tok; const float sxr = sx0[tok];
;                 f32x4 o1[2], o2[2];
; #pragma unroll
;                 for (int n = 0; n < 2; ++n)
; #pragma unroll
;                     for (int j = 0; j < 4; ++j) { float c, s; cs_rev(pos * inv[4 * n + j], c, s); const float x1 = ACCF(ai, 0, m, n, j), x2 = ACCF(ai, 1, m, n, j); o1[n][j] = x1 * c - x2 * s; o2[n][j] = x2 * c + x1 * s; }
;                 if (isq) {
;                     bf16* q = qs + (size_t)tok * RW + h * HD + c0; *(GAS v4u*)q = pack8(o1[0], o1[1]); *(GAS v4u*)(q + 128) = pack8(o2[0], o2[1]);
;                     const int il = r; const float wf = fexp(lgf * (float)(il + 1)), wb = fexp(lgb * (float)(255 - il));
;                     bf16* a = Acat + ((size_t)h * T + tok) * CAT + c0;
;                     *(GAS v4u*)(a + 256) = pack8(o1[0] * wf, o1[1] * wf); *(GAS v4u*)(a + 384) = pack8(o2[0] * wf, o2[1] * wf);
;                     *(GAS v4u*)(a + 512) = pack8(o1[0] * wb, o1[1] * wb); *(GAS v4u*)(a + 640) = pack8(o2[0] * wb, o2[1] * wb);
;                 } else {
;                     bf16* k = kk + (size_t)tok * RW + h * HD + c0; *(GAS v4u*)k = pack8(o1[0] * 0.0625f, o1[1] * 0.0625f); *(GAS v4u*)(k + 128) = pack8(o2[0] * 0.0625f, o2[1] * 0.0625f);
;                 }
.LBB0_189:
	global_store_dwordx4 v[158:159], v[128:131], off
	v_cvt_f32_i32_e32 v125, v125
	v_cvt_f32_i32_e32 v124, v124
	v_add_u32_e32 v128, 16, v144
	v_ashrrev_i32_e32 v129, 31, v128
	v_lshl_add_u64 v[130:131], v[128:129], 2, s[34:35]
	v_mov_b32_e32 v134, v216
	v_cvt_f32_i32_e32 v135, v128
	v_cvt_f32_i32_e32 v121, v121
	v_cvt_f32_i32_e32 v120, v120
	v_cvt_f32_i32_e32 v127, v127
	v_mul_f32_e32 v130, v148, v135
	v_fract_f32_e32 v131, v130
	v_cos_f32_e32 v130, v131
	v_sin_f32_e32 v136, v131
	v_mul_f32_e32 v131, v165, v135
	v_fract_f32_e32 v137, v131
	v_cos_f32_e32 v131, v137
	v_sin_f32_e32 v137, v137
	v_cvt_f32_i32_e32 v126, v126
	v_cvt_f32_i32_e32 v123, v123
	v_cvt_f32_i32_e32 v122, v122
	v_cvt_f32_i32_e32 v117, v117
	v_cvt_f32_i32_e32 v116, v116
	v_cvt_f32_i32_e32 v113, v113
	v_cvt_f32_i32_e32 v112, v112
	v_cvt_f32_i32_e32 v119, v119
	v_cvt_f32_i32_e32 v118, v118
	v_cvt_f32_i32_e32 v115, v115
	v_cvt_f32_i32_e32 v114, v114
	s_mov_b64 s[74:75], -1
	s_andn2_b64 vcc, exec, s[72:73]
	v_pk_mul_f32 v[138:139], v[40:41], v[134:135] op_sel_hi:[1,0]
	s_nop 0
	v_pk_mul_f32 v[124:125], v[138:139], v[124:125]
	v_pk_mul_f32 v[138:139], v[44:45], v[134:135] op_sel_hi:[1,0]
	s_nop 0
	v_pk_mul_f32 v[138:139], v[138:139], v[120:121]
	s_nop 0
	v_pk_mul_f32 v[120:121], v[130:131], v[138:139]
	s_nop 0
	v_pk_fma_f32 v[120:121], v[136:137], v[124:125], v[120:121]
	v_pk_mul_f32 v[136:137], v[136:137], v[138:139]
	v_pk_mul_f32 v[138:139], v[42:43], v[134:135] op_sel_hi:[1,0]
	v_pk_fma_f32 v[124:125], v[130:131], v[124:125], v[136:137] neg_lo:[0,0,1] neg_hi:[0,0,1]
	v_mul_f32_e32 v130, v166, v135
	v_fract_f32_e32 v131, v130
	v_cos_f32_e32 v130, v131
	v_sin_f32_e32 v136, v131
	v_mul_f32_e32 v131, v167, v135
	v_fract_f32_e32 v137, v131
	v_cos_f32_e32 v131, v137
	v_sin_f32_e32 v137, v137
	v_pk_mul_f32 v[126:127], v[138:139], v[126:127]
	v_pk_mul_f32 v[138:139], v[46:47], v[134:135] op_sel_hi:[1,0]
	s_nop 0
	v_pk_mul_f32 v[138:139], v[138:139], v[122:123]
	s_nop 0
	v_pk_mul_f32 v[122:123], v[130:131], v[138:139]
	s_nop 0
	v_pk_fma_f32 v[122:123], v[136:137], v[126:127], v[122:123]
	v_pk_mul_f32 v[136:137], v[136:137], v[138:139]
	v_pk_mul_f32 v[138:139], v[32:33], v[134:135] op_sel_hi:[1,0]
	v_pk_fma_f32 v[126:127], v[130:131], v[126:127], v[136:137] neg_lo:[0,0,1] neg_hi:[0,0,1]
	v_mul_f32_e32 v130, v168, v135
	v_fract_f32_e32 v131, v130
	v_cos_f32_e32 v130, v131
	v_sin_f32_e32 v136, v131
	v_mul_f32_e32 v131, v169, v135
	v_fract_f32_e32 v137, v131
	v_cos_f32_e32 v131, v137
	v_sin_f32_e32 v137, v137
	v_pk_mul_f32 v[138:139], v[138:139], v[116:117]
	v_pk_mul_f32 v[116:117], v[36:37], v[134:135] op_sel_hi:[1,0]
	s_nop 0
	v_pk_mul_f32 v[112:113], v[116:117], v[112:113]
	s_nop 0
	v_pk_mul_f32 v[116:117], v[130:131], v[112:113]
	v_pk_mul_f32 v[112:113], v[136:137], v[112:113]
	v_pk_fma_f32 v[116:117], v[136:137], v[138:139], v[116:117]
	v_pk_fma_f32 v[130:131], v[130:131], v[138:139], v[112:113] neg_lo:[0,0,1] neg_hi:[0,0,1]
	v_mul_f32_e32 v112, v170, v135
	v_fract_f32_e32 v113, v112
	v_cos_f32_e32 v112, v113
	v_sin_f32_e32 v136, v113
	v_mul_f32_e32 v113, v171, v135
	v_fract_f32_e32 v135, v113
	v_cos_f32_e32 v113, v135
	v_sin_f32_e32 v137, v135
	v_pk_mul_f32 v[138:139], v[34:35], v[134:135] op_sel_hi:[1,0]
	s_nop 0
	v_pk_mul_f32 v[138:139], v[138:139], v[118:119]
	v_pk_mul_f32 v[118:119], v[38:39], v[134:135] op_sel_hi:[1,0]
	s_nop 0
	v_pk_mul_f32 v[114:115], v[118:119], v[114:115]
	s_nop 0
	v_pk_mul_f32 v[118:119], v[112:113], v[114:115]
	v_pk_mul_f32 v[114:115], v[136:137], v[114:115]
	v_pk_fma_f32 v[118:119], v[136:137], v[138:139], v[118:119]
	v_pk_fma_f32 v[134:135], v[112:113], v[138:139], v[114:115] neg_lo:[0,0,1] neg_hi:[0,0,1]
	v_cndmask_b32_e64 v112, 0, 1, s[72:73]
	v_lshlrev_b64 v[136:137], 11, v[128:129]
	v_cmp_ne_u32_e64 s[4:5], 1, v112
	s_cbranch_vccnz .LBB0_191
	v_lshl_add_u64 v[112:113], s[40:41], 0, v[136:137]
	s_lshl_b32 s72, s19, 1
	s_mov_b32 s73, s7
	v_lshl_add_u64 v[112:113], v[112:113], 0, s[72:73]
	v_lshl_add_u64 v[138:139], v[150:151], 1, v[112:113]
	v_pk_mul_f32 v[114:115], v[126:127], s[54:55] op_sel_hi:[1,0]
	v_pk_mul_f32 v[112:113], v[124:125], s[54:55] op_sel_hi:[1,0]
	v_pk_mul_f32 v[140:141], v[130:131], s[54:55] op_sel_hi:[1,0]
	v_pk_mul_f32 v[142:143], v[134:135], s[54:55] op_sel_hi:[1,0]
	v_cvt_pk_bf16_f32 v112, v112, v113
	v_cvt_pk_bf16_f32 v113, v114, v115
	v_cvt_pk_bf16_f32 v114, v140, v141
	s_mov_b64 s[74:75], 0
	v_cvt_pk_bf16_f32 v115, v142, v143
	global_store_dwordx4 v[138:139], v[112:115], off
	v_lshl_add_u64 v[138:139], v[138:139], 0, s[52:53]
	v_pk_mul_f32 v[140:141], v[116:117], s[54:55] op_sel_hi:[1,0]
	v_pk_mul_f32 v[114:115], v[122:123], s[54:55] op_sel_hi:[1,0]
	v_pk_mul_f32 v[112:113], v[120:121], s[54:55] op_sel_hi:[1,0]
	v_pk_mul_f32 v[142:143], v[118:119], s[54:55] op_sel_hi:[1,0]
	v_cvt_pk_bf16_f32 v112, v112, v113
	v_cvt_pk_bf16_f32 v113, v114, v115
	v_cvt_pk_bf16_f32 v114, v140, v141
	s_nop 0
	v_cvt_pk_bf16_f32 v115, v142, v143

; #define GAS __attribute__((address_space(1)))
; __device__ __forceinline__ v4u pack8(const f32x4 a, const f32x4 b) { v4u w; w.x = cvt_pk_bf16(a[0], a[1]); w.y = cvt_pk_bf16(a[2], a[3]); w.z = cvt_pk_bf16(b[0], b[1]); w.w = cvt_pk_bf16(b[2], b[3]); return w; }
; __device__ __forceinline__ float fexp(float x) { return __builtin_amdgcn_exp2f(x * 1.4426950408889634f); }
; __device__ __forceinline__ void cs_rev(float rev, float& c, float& s) { const float f = __builtin_amdgcn_fractf(rev); c = __builtin_amdgcn_cosf(f); s = __builtin_amdgcn_sinf(f); }
; #define EPI_LOOP_AM for (int ai = 0; ai < 2; ++ai) _Pragma("unroll") for (int m = 0; m < 4; ++m)
;     __device__ __forceinline__ void operator()(AccI& acci, const Unit& u, LAS unsigned char*, int wr, int wc, int fr, int fq) const {
;     ...
;             EPI_LOOP_AM {
;                 const int r = 128 * ai + 64 * wr + 16 * m + fr, tok = pm * 256 + r; const float pos = (float)tok; const float sxr = sx0[tok];
;                 f32x4 o1[2], o2[2];
; #pragma unroll
;                 for (int n = 0; n < 2; ++n)
; #pragma unroll
;                     for (int j = 0; j < 4; ++j) { float c, s; cs_rev(pos * inv[4 * n + j], c, s); const float x1 = ACCF(ai, 0, m, n, j), x2 = ACCF(ai, 1, m, n, j); o1[n][j] = x1 * c - x2 * s; o2[n][j] = x2 * c + x1 * s; }
;                 if (isq) {
;                     bf16* q = qs + (size_t)tok * RW + h * HD + c0; *(GAS v4u*)q = pack8(o1[0], o1[1]); *(GAS v4u*)(q + 128) = pack8(o2[0], o2[1]);
;                     const int il = r; const float wf = fexp(lgf * (float)(il + 1)), wb = fexp(lgb * (float)(255 - il));
;                     bf16* a = Acat + ((size_t)h * T + tok) * CAT + c0;
;                     *(GAS v4u*)(a + 256) = pack8(o1[0] * wf, o1[1] * wf); *(GAS v4u*)(a + 384) = pack8(o2[0] * wf, o2[1] * wf);
;                     *(GAS v4u*)(a + 512) = pack8(o1[0] * wb, o1[1] * wb); *(GAS v4u*)(a + 640) = pack8(o2[0] * wb, o2[1] * wb);
;                 } else {
;                     bf16* k = kk + (size_t)tok * RW + h * HD + c0; *(GAS v4u*)k = pack8(o1[0] * 0.0625f, o1[1] * 0.0625f); *(GAS v4u*)(k + 128) = pack8(o2[0] * 0.0625f, o2[1] * 0.0625f);
;                 }
.LBB0_193:
	global_store_dwordx4 v[138:139], v[112:115], off
	v_cvt_f32_i32_e32 v109, v109
	v_cvt_f32_i32_e32 v108, v108
	v_add_u32_e32 v112, 32, v144
	v_ashrrev_i32_e32 v113, 31, v112
	v_lshl_add_u64 v[114:115], v[112:113], 2, s[34:35]
	v_mov_b32_e32 v116, v217
	v_cvt_f32_i32_e32 v117, v112
	v_cvt_f32_i32_e32 v105, v105
	v_cvt_f32_i32_e32 v104, v104
	v_cvt_f32_i32_e32 v111, v111
	v_mul_f32_e32 v114, v148, v117
	v_fract_f32_e32 v115, v114
	v_cos_f32_e32 v114, v115
	v_sin_f32_e32 v118, v115
	v_mul_f32_e32 v115, v165, v117
	v_fract_f32_e32 v119, v115
	v_cos_f32_e32 v115, v119
	v_sin_f32_e32 v119, v119
	v_cvt_f32_i32_e32 v110, v110
	v_cvt_f32_i32_e32 v107, v107
	v_cvt_f32_i32_e32 v106, v106
	v_cvt_f32_i32_e32 v101, v101
	v_cvt_f32_i32_e32 v100, v100
	v_cvt_f32_i32_e32 v97, v97
	v_cvt_f32_i32_e32 v96, v96
	v_cvt_f32_i32_e32 v103, v103
	v_cvt_f32_i32_e32 v102, v102
	v_cvt_f32_i32_e32 v99, v99
	v_cvt_f32_i32_e32 v98, v98
	s_mov_b64 s[72:73], -1
	s_and_b64 vcc, exec, s[4:5]
	v_pk_mul_f32 v[120:121], v[40:41], v[116:117] op_sel_hi:[1,0]
	s_nop 0
	v_pk_mul_f32 v[108:109], v[120:121], v[108:109]
	v_pk_mul_f32 v[120:121], v[44:45], v[116:117] op_sel_hi:[1,0]
	s_nop 0
	v_pk_mul_f32 v[120:121], v[120:121], v[104:105]
	s_nop 0
	v_pk_mul_f32 v[104:105], v[114:115], v[120:121]
	s_nop 0
	v_pk_fma_f32 v[104:105], v[118:119], v[108:109], v[104:105]
	v_pk_mul_f32 v[118:119], v[118:119], v[120:121]
	v_pk_mul_f32 v[120:121], v[42:43], v[116:117] op_sel_hi:[1,0]
	v_pk_fma_f32 v[108:109], v[114:115], v[108:109], v[118:119] neg_lo:[0,0,1] neg_hi:[0,0,1]
	v_mul_f32_e32 v114, v166, v117
	v_fract_f32_e32 v115, v114
	v_cos_f32_e32 v114, v115
	v_sin_f32_e32 v118, v115
	v_mul_f32_e32 v115, v167, v117
	v_fract_f32_e32 v119, v115
	v_cos_f32_e32 v115, v119
	v_sin_f32_e32 v119, v119
	v_pk_mul_f32 v[110:111], v[120:121], v[110:111]
	v_pk_mul_f32 v[120:121], v[46:47], v[116:117] op_sel_hi:[1,0]
	s_nop 0
	v_pk_mul_f32 v[120:121], v[120:121], v[106:107]
	s_nop 0
	v_pk_mul_f32 v[106:107], v[114:115], v[120:121]
	s_nop 0
	v_pk_fma_f32 v[106:107], v[118:119], v[110:111], v[106:107]
	v_pk_mul_f32 v[118:119], v[118:119], v[120:121]
	v_pk_mul_f32 v[120:121], v[32:33], v[116:117] op_sel_hi:[1,0]
	v_pk_fma_f32 v[110:111], v[114:115], v[110:111], v[118:119] neg_lo:[0,0,1] neg_hi:[0,0,1]
	v_mul_f32_e32 v114, v168, v117
	v_fract_f32_e32 v115, v114
	v_cos_f32_e32 v114, v115
	v_sin_f32_e32 v118, v115
	v_mul_f32_e32 v115, v169, v117
	v_fract_f32_e32 v119, v115
	v_cos_f32_e32 v115, v119
	v_sin_f32_e32 v119, v119
	v_pk_mul_f32 v[120:121], v[120:121], v[100:101]
	v_pk_mul_f32 v[100:101], v[36:37], v[116:117] op_sel_hi:[1,0]
	s_nop 0
	v_pk_mul_f32 v[96:97], v[100:101], v[96:97]
	s_nop 0
	v_pk_mul_f32 v[100:101], v[114:115], v[96:97]
	v_pk_mul_f32 v[96:97], v[118:119], v[96:97]
	v_pk_fma_f32 v[100:101], v[118:119], v[120:121], v[100:101]
	v_pk_fma_f32 v[114:115], v[114:115], v[120:121], v[96:97] neg_lo:[0,0,1] neg_hi:[0,0,1]
	v_mul_f32_e32 v96, v170, v117
	v_fract_f32_e32 v97, v96
	v_cos_f32_e32 v96, v97
	v_sin_f32_e32 v118, v97
	v_mul_f32_e32 v97, v171, v117
	v_fract_f32_e32 v117, v97
	v_cos_f32_e32 v97, v117
	v_sin_f32_e32 v119, v117
	v_pk_mul_f32 v[120:121], v[34:35], v[116:117] op_sel_hi:[1,0]
	s_nop 0
	v_pk_mul_f32 v[120:121], v[120:121], v[102:103]
	v_pk_mul_f32 v[102:103], v[38:39], v[116:117] op_sel_hi:[1,0]
	s_nop 0
	v_pk_mul_f32 v[98:99], v[102:103], v[98:99]
	s_nop 0
	v_pk_mul_f32 v[102:103], v[96:97], v[98:99]
	v_pk_mul_f32 v[98:99], v[118:119], v[98:99]
	v_pk_fma_f32 v[102:103], v[118:119], v[120:121], v[102:103]
	v_pk_fma_f32 v[116:117], v[96:97], v[120:121], v[98:99] neg_lo:[0,0,1] neg_hi:[0,0,1]
	v_lshlrev_b64 v[118:119], 11, v[112:113]
	s_cbranch_vccnz .LBB0_195
	v_lshl_add_u64 v[96:97], s[40:41], 0, v[118:119]
	s_lshl_b32 s72, s19, 1
	s_mov_b32 s73, s7
	v_lshl_add_u64 v[96:97], v[96:97], 0, s[72:73]
	v_lshl_add_u64 v[120:121], v[150:151], 1, v[96:97]
	v_pk_mul_f32 v[98:99], v[110:111], s[54:55] op_sel_hi:[1,0]
	v_pk_mul_f32 v[96:97], v[108:109], s[54:55] op_sel_hi:[1,0]
	v_pk_mul_f32 v[122:123], v[114:115], s[54:55] op_sel_hi:[1,0]
	v_pk_mul_f32 v[124:125], v[116:117], s[54:55] op_sel_hi:[1,0]
	v_cvt_pk_bf16_f32 v96, v96, v97
	v_cvt_pk_bf16_f32 v97, v98, v99
	v_cvt_pk_bf16_f32 v98, v122, v123
	s_mov_b64 s[72:73], 0
	v_cvt_pk_bf16_f32 v99, v124, v125
	global_store_dwordx4 v[120:121], v[96:99], off
	v_lshl_add_u64 v[120:121], v[120:121], 0, s[52:53]
	v_pk_mul_f32 v[122:123], v[100:101], s[54:55] op_sel_hi:[1,0]
	v_pk_mul_f32 v[98:99], v[106:107], s[54:55] op_sel_hi:[1,0]
	v_pk_mul_f32 v[96:97], v[104:105], s[54:55] op_sel_hi:[1,0]
	v_pk_mul_f32 v[124:125], v[102:103], s[54:55] op_sel_hi:[1,0]
	v_cvt_pk_bf16_f32 v96, v96, v97
	v_cvt_pk_bf16_f32 v97, v98, v99
	v_cvt_pk_bf16_f32 v98, v122, v123
	s_nop 0
	v_cvt_pk_bf16_f32 v99, v124, v125

; #define GAS __attribute__((address_space(1)))
; __device__ __forceinline__ v4u pack8(const f32x4 a, const f32x4 b) { v4u w; w.x = cvt_pk_bf16(a[0], a[1]); w.y = cvt_pk_bf16(a[2], a[3]); w.z = cvt_pk_bf16(b[0], b[1]); w.w = cvt_pk_bf16(b[2], b[3]); return w; }
; __device__ __forceinline__ float fexp(float x) { return __builtin_amdgcn_exp2f(x * 1.4426950408889634f); }
; __device__ __forceinline__ void cs_rev(float rev, float& c, float& s) { const float f = __builtin_amdgcn_fractf(rev); c = __builtin_amdgcn_cosf(f); s = __builtin_amdgcn_sinf(f); }
; #define EPI_LOOP_AM for (int ai = 0; ai < 2; ++ai) _Pragma("unroll") for (int m = 0; m < 4; ++m)
;     __device__ __forceinline__ void operator()(AccI& acci, const Unit& u, LAS unsigned char*, int wr, int wc, int fr, int fq) const {
;     ...
;             EPI_LOOP_AM {
;                 const int r = 128 * ai + 64 * wr + 16 * m + fr, tok = pm * 256 + r; const float pos = (float)tok; const float sxr = sx0[tok];
;                 f32x4 o1[2], o2[2];
; #pragma unroll
;                 for (int n = 0; n < 2; ++n)
; #pragma unroll
;                     for (int j = 0; j < 4; ++j) { float c, s; cs_rev(pos * inv[4 * n + j], c, s); const float x1 = ACCF(ai, 0, m, n, j), x2 = ACCF(ai, 1, m, n, j); o1[n][j] = x1 * c - x2 * s; o2[n][j] = x2 * c + x1 * s; }
;                 if (isq) {
;                     bf16* q = qs + (size_t)tok * RW + h * HD + c0; *(GAS v4u*)q = pack8(o1[0], o1[1]); *(GAS v4u*)(q + 128) = pack8(o2[0], o2[1]);
;                     const int il = r; const float wf = fexp(lgf * (float)(il + 1)), wb = fexp(lgb * (float)(255 - il));
;                     bf16* a = Acat + ((size_t)h * T + tok) * CAT + c0;
;                     *(GAS v4u*)(a + 256) = pack8(o1[0] * wf, o1[1] * wf); *(GAS v4u*)(a + 384) = pack8(o2[0] * wf, o2[1] * wf);
;                     *(GAS v4u*)(a + 512) = pack8(o1[0] * wb, o1[1] * wb); *(GAS v4u*)(a + 640) = pack8(o2[0] * wb, o2[1] * wb);
;                 } else {
;                     bf16* k = kk + (size_t)tok * RW + h * HD + c0; *(GAS v4u*)k = pack8(o1[0] * 0.0625f, o1[1] * 0.0625f); *(GAS v4u*)(k + 128) = pack8(o2[0] * 0.0625f, o2[1] * 0.0625f);
;                 }
.LBB0_197:
	global_store_dwordx4 v[120:121], v[96:99], off
	v_cvt_f32_i32_e32 v93, v93
	v_cvt_f32_i32_e32 v92, v92
	v_add_u32_e32 v96, 48, v144
	v_ashrrev_i32_e32 v97, 31, v96
	v_lshl_add_u64 v[98:99], v[96:97], 2, s[34:35]
	v_mov_b32_e32 v100, v218
	v_cvt_f32_i32_e32 v101, v96
	v_cvt_f32_i32_e32 v89, v89
	v_cvt_f32_i32_e32 v88, v88
	v_cvt_f32_i32_e32 v95, v95
	v_mul_f32_e32 v98, v148, v101
	v_fract_f32_e32 v99, v98
	v_cos_f32_e32 v98, v99
	v_sin_f32_e32 v102, v99
	v_mul_f32_e32 v99, v165, v101
	v_fract_f32_e32 v103, v99
	v_cos_f32_e32 v99, v103
	v_sin_f32_e32 v103, v103
	v_cvt_f32_i32_e32 v94, v94
	v_cvt_f32_i32_e32 v91, v91
	v_cvt_f32_i32_e32 v90, v90
	v_cvt_f32_i32_e32 v85, v85
	v_cvt_f32_i32_e32 v84, v84
	v_cvt_f32_i32_e32 v81, v81
	v_cvt_f32_i32_e32 v80, v80
	v_cvt_f32_i32_e32 v87, v87
	v_cvt_f32_i32_e32 v86, v86
	v_cvt_f32_i32_e32 v83, v83
	v_cvt_f32_i32_e32 v82, v82
	s_mov_b64 s[72:73], -1
	s_and_b64 vcc, exec, s[4:5]
	v_pk_mul_f32 v[104:105], v[40:41], v[100:101] op_sel_hi:[1,0]
	s_nop 0
	v_pk_mul_f32 v[92:93], v[104:105], v[92:93]
	v_pk_mul_f32 v[104:105], v[44:45], v[100:101] op_sel_hi:[1,0]
	s_nop 0
	v_pk_mul_f32 v[104:105], v[104:105], v[88:89]
	s_nop 0
	v_pk_mul_f32 v[88:89], v[98:99], v[104:105]
	s_nop 0
	v_pk_fma_f32 v[88:89], v[102:103], v[92:93], v[88:89]
	v_pk_mul_f32 v[102:103], v[102:103], v[104:105]
	v_pk_mul_f32 v[104:105], v[42:43], v[100:101] op_sel_hi:[1,0]
	v_pk_fma_f32 v[92:93], v[98:99], v[92:93], v[102:103] neg_lo:[0,0,1] neg_hi:[0,0,1]
	v_mul_f32_e32 v98, v166, v101
	v_fract_f32_e32 v99, v98
	v_cos_f32_e32 v98, v99
	v_sin_f32_e32 v102, v99
	v_mul_f32_e32 v99, v167, v101
	v_fract_f32_e32 v103, v99
	v_cos_f32_e32 v99, v103
	v_sin_f32_e32 v103, v103
	v_pk_mul_f32 v[94:95], v[104:105], v[94:95]
	v_pk_mul_f32 v[104:105], v[46:47], v[100:101] op_sel_hi:[1,0]
	s_nop 0
	v_pk_mul_f32 v[104:105], v[104:105], v[90:91]
	s_nop 0
	v_pk_mul_f32 v[90:91], v[98:99], v[104:105]
	s_nop 0
	v_pk_fma_f32 v[90:91], v[102:103], v[94:95], v[90:91]
	v_pk_mul_f32 v[102:103], v[102:103], v[104:105]
	v_pk_mul_f32 v[104:105], v[32:33], v[100:101] op_sel_hi:[1,0]
	v_pk_fma_f32 v[94:95], v[98:99], v[94:95], v[102:103] neg_lo:[0,0,1] neg_hi:[0,0,1]
	v_mul_f32_e32 v98, v168, v101
	v_fract_f32_e32 v99, v98
	v_cos_f32_e32 v98, v99
	v_sin_f32_e32 v102, v99
	v_mul_f32_e32 v99, v169, v101
	v_fract_f32_e32 v103, v99
	v_cos_f32_e32 v99, v103
	v_sin_f32_e32 v103, v103
	v_pk_mul_f32 v[104:105], v[104:105], v[84:85]
	v_pk_mul_f32 v[84:85], v[36:37], v[100:101] op_sel_hi:[1,0]
	s_nop 0
	v_pk_mul_f32 v[80:81], v[84:85], v[80:81]
	s_nop 0
	v_pk_mul_f32 v[84:85], v[98:99], v[80:81]
	v_pk_mul_f32 v[80:81], v[102:103], v[80:81]
	v_pk_fma_f32 v[84:85], v[102:103], v[104:105], v[84:85]
	v_pk_fma_f32 v[98:99], v[98:99], v[104:105], v[80:81] neg_lo:[0,0,1] neg_hi:[0,0,1]
	v_mul_f32_e32 v80, v170, v101
	v_fract_f32_e32 v81, v80
	v_cos_f32_e32 v80, v81
	v_sin_f32_e32 v102, v81
	v_mul_f32_e32 v81, v171, v101
	v_fract_f32_e32 v101, v81
	v_cos_f32_e32 v81, v101
	v_sin_f32_e32 v103, v101
	v_pk_mul_f32 v[104:105], v[34:35], v[100:101] op_sel_hi:[1,0]
	s_nop 0
	v_pk_mul_f32 v[104:105], v[104:105], v[86:87]
	v_pk_mul_f32 v[86:87], v[38:39], v[100:101] op_sel_hi:[1,0]
	s_nop 0
	v_pk_mul_f32 v[82:83], v[86:87], v[82:83]
	s_nop 0
	v_pk_mul_f32 v[86:87], v[80:81], v[82:83]
	v_pk_mul_f32 v[82:83], v[102:103], v[82:83]
	v_pk_fma_f32 v[86:87], v[102:103], v[104:105], v[86:87]
	v_pk_fma_f32 v[100:101], v[80:81], v[104:105], v[82:83] neg_lo:[0,0,1] neg_hi:[0,0,1]
	v_lshlrev_b64 v[102:103], 11, v[96:97]
	s_cbranch_vccnz .LBB0_199
	v_lshl_add_u64 v[80:81], s[40:41], 0, v[102:103]
	s_lshl_b32 s72, s19, 1
	s_mov_b32 s73, s7
	v_lshl_add_u64 v[80:81], v[80:81], 0, s[72:73]
	v_lshl_add_u64 v[104:105], v[150:151], 1, v[80:81]
	v_pk_mul_f32 v[82:83], v[94:95], s[54:55] op_sel_hi:[1,0]
	v_pk_mul_f32 v[80:81], v[92:93], s[54:55] op_sel_hi:[1,0]
	v_pk_mul_f32 v[106:107], v[98:99], s[54:55] op_sel_hi:[1,0]
	v_pk_mul_f32 v[108:109], v[100:101], s[54:55] op_sel_hi:[1,0]
	v_cvt_pk_bf16_f32 v80, v80, v81
	v_cvt_pk_bf16_f32 v81, v82, v83
	v_cvt_pk_bf16_f32 v82, v106, v107
	s_mov_b64 s[72:73], 0
	v_cvt_pk_bf16_f32 v83, v108, v109
	global_store_dwordx4 v[104:105], v[80:83], off
	v_lshl_add_u64 v[104:105], v[104:105], 0, s[52:53]
	v_pk_mul_f32 v[106:107], v[84:85], s[54:55] op_sel_hi:[1,0]
	v_pk_mul_f32 v[82:83], v[90:91], s[54:55] op_sel_hi:[1,0]
	v_pk_mul_f32 v[80:81], v[88:89], s[54:55] op_sel_hi:[1,0]
	v_pk_mul_f32 v[108:109], v[86:87], s[54:55] op_sel_hi:[1,0]
	v_cvt_pk_bf16_f32 v80, v80, v81
	v_cvt_pk_bf16_f32 v81, v82, v83
	v_cvt_pk_bf16_f32 v82, v106, v107
	s_nop 0
	v_cvt_pk_bf16_f32 v83, v108, v109

; #define GAS __attribute__((address_space(1)))
; __device__ __forceinline__ v4u pack8(const f32x4 a, const f32x4 b) { v4u w; w.x = cvt_pk_bf16(a[0], a[1]); w.y = cvt_pk_bf16(a[2], a[3]); w.z = cvt_pk_bf16(b[0], b[1]); w.w = cvt_pk_bf16(b[2], b[3]); return w; }
; __device__ __forceinline__ float fexp(float x) { return __builtin_amdgcn_exp2f(x * 1.4426950408889634f); }
; __device__ __forceinline__ void cs_rev(float rev, float& c, float& s) { const float f = __builtin_amdgcn_fractf(rev); c = __builtin_amdgcn_cosf(f); s = __builtin_amdgcn_sinf(f); }
; #define EPI_LOOP_AM for (int ai = 0; ai < 2; ++ai) _Pragma("unroll") for (int m = 0; m < 4; ++m)
;     __device__ __forceinline__ void operator()(AccI& acci, const Unit& u, LAS unsigned char*, int wr, int wc, int fr, int fq) const {
;     ...
;             EPI_LOOP_AM {
;                 const int r = 128 * ai + 64 * wr + 16 * m + fr, tok = pm * 256 + r; const float pos = (float)tok; const float sxr = sx0[tok];
;                 f32x4 o1[2], o2[2];
; #pragma unroll
;                 for (int n = 0; n < 2; ++n)
; #pragma unroll
;                     for (int j = 0; j < 4; ++j) { float c, s; cs_rev(pos * inv[4 * n + j], c, s); const float x1 = ACCF(ai, 0, m, n, j), x2 = ACCF(ai, 1, m, n, j); o1[n][j] = x1 * c - x2 * s; o2[n][j] = x2 * c + x1 * s; }
;                 if (isq) {
;                     bf16* q = qs + (size_t)tok * RW + h * HD + c0; *(GAS v4u*)q = pack8(o1[0], o1[1]); *(GAS v4u*)(q + 128) = pack8(o2[0], o2[1]);
;                     const int il = r; const float wf = fexp(lgf * (float)(il + 1)), wb = fexp(lgb * (float)(255 - il));
;                     bf16* a = Acat + ((size_t)h * T + tok) * CAT + c0;
;                     *(GAS v4u*)(a + 256) = pack8(o1[0] * wf, o1[1] * wf); *(GAS v4u*)(a + 384) = pack8(o2[0] * wf, o2[1] * wf);
;                     *(GAS v4u*)(a + 512) = pack8(o1[0] * wb, o1[1] * wb); *(GAS v4u*)(a + 640) = pack8(o2[0] * wb, o2[1] * wb);
;                 } else {
;                     bf16* k = kk + (size_t)tok * RW + h * HD + c0; *(GAS v4u*)k = pack8(o1[0] * 0.0625f, o1[1] * 0.0625f); *(GAS v4u*)(k + 128) = pack8(o2[0] * 0.0625f, o2[1] * 0.0625f);
;                 }
.LBB0_201:
	global_store_dwordx4 v[104:105], v[80:83], off
	v_cvt_f32_i32_e32 v77, v77
	v_cvt_f32_i32_e32 v76, v76
	v_add_u32_e32 v80, 0x80, v144
	v_ashrrev_i32_e32 v81, 31, v80
	v_lshl_add_u64 v[82:83], v[80:81], 2, s[34:35]
	v_mov_b32_e32 v84, v219
	v_cvt_f32_i32_e32 v85, v80
	v_cvt_f32_i32_e32 v73, v73
	v_cvt_f32_i32_e32 v72, v72
	v_cvt_f32_i32_e32 v79, v79
	v_mul_f32_e32 v82, v148, v85
	v_fract_f32_e32 v83, v82
	v_cos_f32_e32 v82, v83
	v_sin_f32_e32 v86, v83
	v_mul_f32_e32 v83, v165, v85
	v_fract_f32_e32 v87, v83
	v_cos_f32_e32 v83, v87
	v_sin_f32_e32 v87, v87
	v_cvt_f32_i32_e32 v78, v78
	v_cvt_f32_i32_e32 v75, v75
	v_cvt_f32_i32_e32 v74, v74
	v_cvt_f32_i32_e32 v69, v69
	v_cvt_f32_i32_e32 v68, v68
	v_cvt_f32_i32_e32 v65, v65
	v_cvt_f32_i32_e32 v64, v64
	v_cvt_f32_i32_e32 v71, v71
	v_cvt_f32_i32_e32 v70, v70
	v_cvt_f32_i32_e32 v67, v67
	v_cvt_f32_i32_e32 v66, v66
	s_mov_b64 s[72:73], -1
	s_and_b64 vcc, exec, s[4:5]
	v_pk_mul_f32 v[88:89], v[40:41], v[84:85] op_sel_hi:[1,0]
	s_nop 0
	v_pk_mul_f32 v[76:77], v[88:89], v[76:77]
	v_pk_mul_f32 v[88:89], v[44:45], v[84:85] op_sel_hi:[1,0]
	s_nop 0
	v_pk_mul_f32 v[88:89], v[88:89], v[72:73]
	s_nop 0
	v_pk_mul_f32 v[72:73], v[82:83], v[88:89]
	s_nop 0
	v_pk_fma_f32 v[72:73], v[86:87], v[76:77], v[72:73]
	v_pk_mul_f32 v[86:87], v[86:87], v[88:89]
	v_pk_mul_f32 v[88:89], v[42:43], v[84:85] op_sel_hi:[1,0]
	v_pk_fma_f32 v[76:77], v[82:83], v[76:77], v[86:87] neg_lo:[0,0,1] neg_hi:[0,0,1]
	v_mul_f32_e32 v82, v166, v85
	v_fract_f32_e32 v83, v82
	v_cos_f32_e32 v82, v83
	v_sin_f32_e32 v86, v83
	v_mul_f32_e32 v83, v167, v85
	v_fract_f32_e32 v87, v83
	v_cos_f32_e32 v83, v87
	v_sin_f32_e32 v87, v87
	v_pk_mul_f32 v[78:79], v[88:89], v[78:79]
	v_pk_mul_f32 v[88:89], v[46:47], v[84:85] op_sel_hi:[1,0]
	s_nop 0
	v_pk_mul_f32 v[88:89], v[88:89], v[74:75]
	s_nop 0
	v_pk_mul_f32 v[74:75], v[82:83], v[88:89]
	s_nop 0
	v_pk_fma_f32 v[74:75], v[86:87], v[78:79], v[74:75]
	v_pk_mul_f32 v[86:87], v[86:87], v[88:89]
	v_pk_mul_f32 v[88:89], v[32:33], v[84:85] op_sel_hi:[1,0]
	v_pk_fma_f32 v[78:79], v[82:83], v[78:79], v[86:87] neg_lo:[0,0,1] neg_hi:[0,0,1]
	v_mul_f32_e32 v82, v168, v85
	v_fract_f32_e32 v83, v82
	v_cos_f32_e32 v82, v83
	v_sin_f32_e32 v86, v83
	v_mul_f32_e32 v83, v169, v85
	v_fract_f32_e32 v87, v83
	v_cos_f32_e32 v83, v87
	v_sin_f32_e32 v87, v87
	v_pk_mul_f32 v[88:89], v[88:89], v[68:69]
	v_pk_mul_f32 v[68:69], v[36:37], v[84:85] op_sel_hi:[1,0]
	s_nop 0
	v_pk_mul_f32 v[64:65], v[68:69], v[64:65]
	s_nop 0
	v_pk_mul_f32 v[68:69], v[82:83], v[64:65]
	v_pk_mul_f32 v[64:65], v[86:87], v[64:65]
	v_pk_fma_f32 v[68:69], v[86:87], v[88:89], v[68:69]
	v_pk_fma_f32 v[82:83], v[82:83], v[88:89], v[64:65] neg_lo:[0,0,1] neg_hi:[0,0,1]
	v_mul_f32_e32 v64, v170, v85
	v_fract_f32_e32 v65, v64
	v_cos_f32_e32 v64, v65
	v_sin_f32_e32 v86, v65
	v_mul_f32_e32 v65, v171, v85
	v_fract_f32_e32 v85, v65
	v_cos_f32_e32 v65, v85
	v_sin_f32_e32 v87, v85
	v_pk_mul_f32 v[88:89], v[34:35], v[84:85] op_sel_hi:[1,0]
	s_nop 0
	v_pk_mul_f32 v[88:89], v[88:89], v[70:71]
	v_pk_mul_f32 v[70:71], v[38:39], v[84:85] op_sel_hi:[1,0]
	s_nop 0
	v_pk_mul_f32 v[66:67], v[70:71], v[66:67]
	s_nop 0
	v_pk_mul_f32 v[70:71], v[64:65], v[66:67]
	v_pk_mul_f32 v[66:67], v[86:87], v[66:67]
	v_pk_fma_f32 v[70:71], v[86:87], v[88:89], v[70:71]
	v_pk_fma_f32 v[84:85], v[64:65], v[88:89], v[66:67] neg_lo:[0,0,1] neg_hi:[0,0,1]
	v_lshlrev_b64 v[86:87], 11, v[80:81]
	s_cbranch_vccnz .LBB0_203
	v_lshl_add_u64 v[64:65], s[40:41], 0, v[86:87]
	s_lshl_b32 s72, s19, 1
	s_mov_b32 s73, s7
	v_lshl_add_u64 v[64:65], v[64:65], 0, s[72:73]
	v_lshl_add_u64 v[88:89], v[150:151], 1, v[64:65]
	v_pk_mul_f32 v[66:67], v[78:79], s[54:55] op_sel_hi:[1,0]
	v_pk_mul_f32 v[64:65], v[76:77], s[54:55] op_sel_hi:[1,0]
	v_pk_mul_f32 v[90:91], v[82:83], s[54:55] op_sel_hi:[1,0]
	v_pk_mul_f32 v[92:93], v[84:85], s[54:55] op_sel_hi:[1,0]
	v_cvt_pk_bf16_f32 v64, v64, v65
	v_cvt_pk_bf16_f32 v65, v66, v67
	v_cvt_pk_bf16_f32 v66, v90, v91
	s_mov_b64 s[72:73], 0
	v_cvt_pk_bf16_f32 v67, v92, v93
	global_store_dwordx4 v[88:89], v[64:67], off
	v_lshl_add_u64 v[88:89], v[88:89], 0, s[52:53]
	v_pk_mul_f32 v[90:91], v[68:69], s[54:55] op_sel_hi:[1,0]
	v_pk_mul_f32 v[66:67], v[74:75], s[54:55] op_sel_hi:[1,0]
	v_pk_mul_f32 v[64:65], v[72:73], s[54:55] op_sel_hi:[1,0]
	v_pk_mul_f32 v[92:93], v[70:71], s[54:55] op_sel_hi:[1,0]
	v_cvt_pk_bf16_f32 v64, v64, v65
	v_cvt_pk_bf16_f32 v65, v66, v67
	v_cvt_pk_bf16_f32 v66, v90, v91
	s_nop 0
	v_cvt_pk_bf16_f32 v67, v92, v93

; #define GAS __attribute__((address_space(1)))
; __device__ __forceinline__ v4u pack8(const f32x4 a, const f32x4 b) { v4u w; w.x = cvt_pk_bf16(a[0], a[1]); w.y = cvt_pk_bf16(a[2], a[3]); w.z = cvt_pk_bf16(b[0], b[1]); w.w = cvt_pk_bf16(b[2], b[3]); return w; }
; __device__ __forceinline__ float fexp(float x) { return __builtin_amdgcn_exp2f(x * 1.4426950408889634f); }
; __device__ __forceinline__ void cs_rev(float rev, float& c, float& s) { const float f = __builtin_amdgcn_fractf(rev); c = __builtin_amdgcn_cosf(f); s = __builtin_amdgcn_sinf(f); }
; #define EPI_LOOP_AM for (int ai = 0; ai < 2; ++ai) _Pragma("unroll") for (int m = 0; m < 4; ++m)
;     __device__ __forceinline__ void operator()(AccI& acci, const Unit& u, LAS unsigned char*, int wr, int wc, int fr, int fq) const {
;     ...
;             EPI_LOOP_AM {
;                 const int r = 128 * ai + 64 * wr + 16 * m + fr, tok = pm * 256 + r; const float pos = (float)tok; const float sxr = sx0[tok];
;                 f32x4 o1[2], o2[2];
; #pragma unroll
;                 for (int n = 0; n < 2; ++n)
; #pragma unroll
;                     for (int j = 0; j < 4; ++j) { float c, s; cs_rev(pos * inv[4 * n + j], c, s); const float x1 = ACCF(ai, 0, m, n, j), x2 = ACCF(ai, 1, m, n, j); o1[n][j] = x1 * c - x2 * s; o2[n][j] = x2 * c + x1 * s; }
;                 if (isq) {
;                     bf16* q = qs + (size_t)tok * RW + h * HD + c0; *(GAS v4u*)q = pack8(o1[0], o1[1]); *(GAS v4u*)(q + 128) = pack8(o2[0], o2[1]);
;                     const int il = r; const float wf = fexp(lgf * (float)(il + 1)), wb = fexp(lgb * (float)(255 - il));
;                     bf16* a = Acat + ((size_t)h * T + tok) * CAT + c0;
;                     *(GAS v4u*)(a + 256) = pack8(o1[0] * wf, o1[1] * wf); *(GAS v4u*)(a + 384) = pack8(o2[0] * wf, o2[1] * wf);
;                     *(GAS v4u*)(a + 512) = pack8(o1[0] * wb, o1[1] * wb); *(GAS v4u*)(a + 640) = pack8(o2[0] * wb, o2[1] * wb);
;                 } else {
;                     bf16* k = kk + (size_t)tok * RW + h * HD + c0; *(GAS v4u*)k = pack8(o1[0] * 0.0625f, o1[1] * 0.0625f); *(GAS v4u*)(k + 128) = pack8(o2[0] * 0.0625f, o2[1] * 0.0625f);
;                 }
.LBB0_205:
	global_store_dwordx4 v[88:89], v[64:67], off
	v_cvt_f32_i32_e32 v61, v61
	v_cvt_f32_i32_e32 v60, v60
	v_add_u32_e32 v64, 0x90, v144
	v_ashrrev_i32_e32 v65, 31, v64
	v_lshl_add_u64 v[66:67], v[64:65], 2, s[34:35]
	v_mov_b32_e32 v68, v220
	v_cvt_f32_i32_e32 v69, v64
	v_cvt_f32_i32_e32 v57, v57
	v_cvt_f32_i32_e32 v56, v56
	v_cvt_f32_i32_e32 v63, v63
	v_mul_f32_e32 v66, v148, v69
	v_fract_f32_e32 v67, v66
	v_cos_f32_e32 v66, v67
	v_sin_f32_e32 v70, v67
	v_mul_f32_e32 v67, v165, v69
	v_fract_f32_e32 v71, v67
	v_cos_f32_e32 v67, v71
	v_sin_f32_e32 v71, v71
	v_cvt_f32_i32_e32 v62, v62
	v_cvt_f32_i32_e32 v59, v59
	v_cvt_f32_i32_e32 v58, v58
	v_cvt_f32_i32_e32 v53, v53
	v_cvt_f32_i32_e32 v52, v52
	v_cvt_f32_i32_e32 v49, v49
	v_cvt_f32_i32_e32 v48, v48
	v_cvt_f32_i32_e32 v55, v55
	v_cvt_f32_i32_e32 v54, v54
	v_cvt_f32_i32_e32 v51, v51
	v_cvt_f32_i32_e32 v50, v50
	s_mov_b64 s[72:73], -1
	s_and_b64 vcc, exec, s[4:5]
	v_pk_mul_f32 v[72:73], v[40:41], v[68:69] op_sel_hi:[1,0]
	s_nop 0
	v_pk_mul_f32 v[60:61], v[72:73], v[60:61]
	v_pk_mul_f32 v[72:73], v[44:45], v[68:69] op_sel_hi:[1,0]
	s_nop 0
	v_pk_mul_f32 v[72:73], v[72:73], v[56:57]
	s_nop 0
	v_pk_mul_f32 v[56:57], v[66:67], v[72:73]
	s_nop 0
	v_pk_fma_f32 v[56:57], v[70:71], v[60:61], v[56:57]
	v_pk_mul_f32 v[70:71], v[70:71], v[72:73]
	v_pk_mul_f32 v[72:73], v[42:43], v[68:69] op_sel_hi:[1,0]
	v_pk_fma_f32 v[60:61], v[66:67], v[60:61], v[70:71] neg_lo:[0,0,1] neg_hi:[0,0,1]
	v_mul_f32_e32 v66, v166, v69
	v_fract_f32_e32 v67, v66
	v_cos_f32_e32 v66, v67
	v_sin_f32_e32 v70, v67
	v_mul_f32_e32 v67, v167, v69
	v_fract_f32_e32 v71, v67
	v_cos_f32_e32 v67, v71
	v_sin_f32_e32 v71, v71
	v_pk_mul_f32 v[62:63], v[72:73], v[62:63]
	v_pk_mul_f32 v[72:73], v[46:47], v[68:69] op_sel_hi:[1,0]
	s_nop 0
	v_pk_mul_f32 v[72:73], v[72:73], v[58:59]
	s_nop 0
	v_pk_mul_f32 v[58:59], v[66:67], v[72:73]
	s_nop 0
	v_pk_fma_f32 v[58:59], v[70:71], v[62:63], v[58:59]
	v_pk_mul_f32 v[70:71], v[70:71], v[72:73]
	v_pk_mul_f32 v[72:73], v[32:33], v[68:69] op_sel_hi:[1,0]
	v_pk_fma_f32 v[62:63], v[66:67], v[62:63], v[70:71] neg_lo:[0,0,1] neg_hi:[0,0,1]
	v_mul_f32_e32 v66, v168, v69
	v_fract_f32_e32 v67, v66
	v_cos_f32_e32 v66, v67
	v_sin_f32_e32 v70, v67
	v_mul_f32_e32 v67, v169, v69
	v_fract_f32_e32 v71, v67
	v_cos_f32_e32 v67, v71
	v_sin_f32_e32 v71, v71
	v_pk_mul_f32 v[72:73], v[72:73], v[52:53]
	v_pk_mul_f32 v[52:53], v[36:37], v[68:69] op_sel_hi:[1,0]
	s_nop 0
	v_pk_mul_f32 v[48:49], v[52:53], v[48:49]
	s_nop 0
	v_pk_mul_f32 v[52:53], v[66:67], v[48:49]
	v_pk_mul_f32 v[48:49], v[70:71], v[48:49]
	v_pk_fma_f32 v[52:53], v[70:71], v[72:73], v[52:53]
	v_pk_fma_f32 v[66:67], v[66:67], v[72:73], v[48:49] neg_lo:[0,0,1] neg_hi:[0,0,1]
	v_mul_f32_e32 v48, v170, v69
	v_fract_f32_e32 v49, v48
	v_cos_f32_e32 v48, v49
	v_sin_f32_e32 v70, v49
	v_mul_f32_e32 v49, v171, v69
	v_fract_f32_e32 v69, v49
	v_cos_f32_e32 v49, v69
	v_sin_f32_e32 v71, v69
	v_pk_mul_f32 v[72:73], v[34:35], v[68:69] op_sel_hi:[1,0]
	s_nop 0
	v_pk_mul_f32 v[72:73], v[72:73], v[54:55]
	v_pk_mul_f32 v[54:55], v[38:39], v[68:69] op_sel_hi:[1,0]
	s_nop 0
	v_pk_mul_f32 v[50:51], v[54:55], v[50:51]
	s_nop 0
	v_pk_mul_f32 v[54:55], v[48:49], v[50:51]
	v_pk_mul_f32 v[50:51], v[70:71], v[50:51]
	v_pk_fma_f32 v[54:55], v[70:71], v[72:73], v[54:55]
	v_pk_fma_f32 v[68:69], v[48:49], v[72:73], v[50:51] neg_lo:[0,0,1] neg_hi:[0,0,1]
	v_lshlrev_b64 v[70:71], 11, v[64:65]
	s_cbranch_vccnz .LBB0_207
	v_lshl_add_u64 v[48:49], s[40:41], 0, v[70:71]
	s_lshl_b32 s72, s19, 1
	s_mov_b32 s73, s7
	v_lshl_add_u64 v[48:49], v[48:49], 0, s[72:73]
	v_lshl_add_u64 v[72:73], v[150:151], 1, v[48:49]
	v_pk_mul_f32 v[50:51], v[62:63], s[54:55] op_sel_hi:[1,0]
	v_pk_mul_f32 v[48:49], v[60:61], s[54:55] op_sel_hi:[1,0]
	v_pk_mul_f32 v[74:75], v[66:67], s[54:55] op_sel_hi:[1,0]
	v_pk_mul_f32 v[76:77], v[68:69], s[54:55] op_sel_hi:[1,0]
	v_cvt_pk_bf16_f32 v48, v48, v49
	v_cvt_pk_bf16_f32 v49, v50, v51
	v_cvt_pk_bf16_f32 v50, v74, v75
	s_mov_b64 s[72:73], 0
	v_cvt_pk_bf16_f32 v51, v76, v77
	global_store_dwordx4 v[72:73], v[48:51], off
	v_lshl_add_u64 v[72:73], v[72:73], 0, s[52:53]
	v_pk_mul_f32 v[74:75], v[52:53], s[54:55] op_sel_hi:[1,0]
	v_pk_mul_f32 v[50:51], v[58:59], s[54:55] op_sel_hi:[1,0]
	v_pk_mul_f32 v[48:49], v[56:57], s[54:55] op_sel_hi:[1,0]
	v_pk_mul_f32 v[76:77], v[54:55], s[54:55] op_sel_hi:[1,0]
	v_cvt_pk_bf16_f32 v48, v48, v49
	v_cvt_pk_bf16_f32 v49, v50, v51
	v_cvt_pk_bf16_f32 v50, v74, v75
	s_nop 0
	v_cvt_pk_bf16_f32 v51, v76, v77

; #define GAS __attribute__((address_space(1)))
; __device__ __forceinline__ v4u pack8(const f32x4 a, const f32x4 b) { v4u w; w.x = cvt_pk_bf16(a[0], a[1]); w.y = cvt_pk_bf16(a[2], a[3]); w.z = cvt_pk_bf16(b[0], b[1]); w.w = cvt_pk_bf16(b[2], b[3]); return w; }
; __device__ __forceinline__ float fexp(float x) { return __builtin_amdgcn_exp2f(x * 1.4426950408889634f); }
; __device__ __forceinline__ void cs_rev(float rev, float& c, float& s) { const float f = __builtin_amdgcn_fractf(rev); c = __builtin_amdgcn_cosf(f); s = __builtin_amdgcn_sinf(f); }
; #define EPI_LOOP_AM for (int ai = 0; ai < 2; ++ai) _Pragma("unroll") for (int m = 0; m < 4; ++m)
;     __device__ __forceinline__ void operator()(AccI& acci, const Unit& u, LAS unsigned char*, int wr, int wc, int fr, int fq) const {
;     ...
;             EPI_LOOP_AM {
;                 const int r = 128 * ai + 64 * wr + 16 * m + fr, tok = pm * 256 + r; const float pos = (float)tok; const float sxr = sx0[tok];
;                 f32x4 o1[2], o2[2];
; #pragma unroll
;                 for (int n = 0; n < 2; ++n)
; #pragma unroll
;                     for (int j = 0; j < 4; ++j) { float c, s; cs_rev(pos * inv[4 * n + j], c, s); const float x1 = ACCF(ai, 0, m, n, j), x2 = ACCF(ai, 1, m, n, j); o1[n][j] = x1 * c - x2 * s; o2[n][j] = x2 * c + x1 * s; }
;                 if (isq) {
;                     bf16* q = qs + (size_t)tok * RW + h * HD + c0; *(GAS v4u*)q = pack8(o1[0], o1[1]); *(GAS v4u*)(q + 128) = pack8(o2[0], o2[1]);
;                     const int il = r; const float wf = fexp(lgf * (float)(il + 1)), wb = fexp(lgb * (float)(255 - il));
;                     bf16* a = Acat + ((size_t)h * T + tok) * CAT + c0;
;                     *(GAS v4u*)(a + 256) = pack8(o1[0] * wf, o1[1] * wf); *(GAS v4u*)(a + 384) = pack8(o2[0] * wf, o2[1] * wf);
;                     *(GAS v4u*)(a + 512) = pack8(o1[0] * wb, o1[1] * wb); *(GAS v4u*)(a + 640) = pack8(o2[0] * wb, o2[1] * wb);
;                 } else {
;                     bf16* k = kk + (size_t)tok * RW + h * HD + c0; *(GAS v4u*)k = pack8(o1[0] * 0.0625f, o1[1] * 0.0625f); *(GAS v4u*)(k + 128) = pack8(o2[0] * 0.0625f, o2[1] * 0.0625f);
;                 }
.LBB0_209:
	global_store_dwordx4 v[72:73], v[48:51], off
	v_cvt_f32_i32_e32 v29, v29
	v_cvt_f32_i32_e32 v28, v28
	v_add_u32_e32 v48, 0xa0, v144
	v_ashrrev_i32_e32 v49, 31, v48
	v_lshl_add_u64 v[50:51], v[48:49], 2, s[34:35]
	v_mov_b32_e32 v52, v221
	v_cvt_f32_i32_e32 v53, v48
	v_cvt_f32_i32_e32 v25, v25
	v_cvt_f32_i32_e32 v24, v24
	v_cvt_f32_i32_e32 v31, v31
	v_mul_f32_e32 v50, v148, v53
	v_fract_f32_e32 v51, v50
	v_cos_f32_e32 v50, v51
	v_sin_f32_e32 v54, v51
	v_mul_f32_e32 v51, v165, v53
	v_fract_f32_e32 v55, v51
	v_cos_f32_e32 v51, v55
	v_sin_f32_e32 v55, v55
	v_cvt_f32_i32_e32 v30, v30
	v_cvt_f32_i32_e32 v27, v27
	v_cvt_f32_i32_e32 v26, v26
	v_cvt_f32_i32_e32 v21, v21
	v_cvt_f32_i32_e32 v20, v20
	v_cvt_f32_i32_e32 v17, v17
	v_cvt_f32_i32_e32 v16, v16
	v_cvt_f32_i32_e32 v23, v23
	v_cvt_f32_i32_e32 v22, v22
	v_cvt_f32_i32_e32 v19, v19
	v_cvt_f32_i32_e32 v18, v18
	s_mov_b64 s[72:73], -1
	s_and_b64 vcc, exec, s[4:5]
	v_pk_mul_f32 v[56:57], v[40:41], v[52:53] op_sel_hi:[1,0]
	s_nop 0
	v_pk_mul_f32 v[28:29], v[56:57], v[28:29]
	v_pk_mul_f32 v[56:57], v[44:45], v[52:53] op_sel_hi:[1,0]
	s_nop 0
	v_pk_mul_f32 v[56:57], v[56:57], v[24:25]
	s_nop 0
	v_pk_mul_f32 v[24:25], v[50:51], v[56:57]
	s_nop 0
	v_pk_fma_f32 v[24:25], v[54:55], v[28:29], v[24:25]
	v_pk_mul_f32 v[54:55], v[54:55], v[56:57]
	v_pk_mul_f32 v[56:57], v[42:43], v[52:53] op_sel_hi:[1,0]
	v_pk_fma_f32 v[28:29], v[50:51], v[28:29], v[54:55] neg_lo:[0,0,1] neg_hi:[0,0,1]
	v_mul_f32_e32 v50, v166, v53
	v_fract_f32_e32 v51, v50
	v_cos_f32_e32 v50, v51
	v_sin_f32_e32 v54, v51
	v_mul_f32_e32 v51, v167, v53
	v_fract_f32_e32 v55, v51
	v_cos_f32_e32 v51, v55
	v_sin_f32_e32 v55, v55
	v_pk_mul_f32 v[30:31], v[56:57], v[30:31]
	v_pk_mul_f32 v[56:57], v[46:47], v[52:53] op_sel_hi:[1,0]
	s_nop 0
	v_pk_mul_f32 v[56:57], v[56:57], v[26:27]
	s_nop 0
	v_pk_mul_f32 v[26:27], v[50:51], v[56:57]
	s_nop 0
	v_pk_fma_f32 v[26:27], v[54:55], v[30:31], v[26:27]
	v_pk_mul_f32 v[54:55], v[54:55], v[56:57]
	v_pk_mul_f32 v[56:57], v[32:33], v[52:53] op_sel_hi:[1,0]
	v_pk_fma_f32 v[30:31], v[50:51], v[30:31], v[54:55] neg_lo:[0,0,1] neg_hi:[0,0,1]
	v_mul_f32_e32 v50, v168, v53
	v_fract_f32_e32 v51, v50
	v_cos_f32_e32 v50, v51
	v_sin_f32_e32 v54, v51
	v_mul_f32_e32 v51, v169, v53
	v_fract_f32_e32 v55, v51
	v_cos_f32_e32 v51, v55
	v_sin_f32_e32 v55, v55
	v_pk_mul_f32 v[56:57], v[56:57], v[20:21]
	v_pk_mul_f32 v[20:21], v[36:37], v[52:53] op_sel_hi:[1,0]
	s_nop 0
	v_pk_mul_f32 v[16:17], v[20:21], v[16:17]
	s_nop 0
	v_pk_mul_f32 v[20:21], v[50:51], v[16:17]
	v_pk_mul_f32 v[16:17], v[54:55], v[16:17]
	v_pk_fma_f32 v[20:21], v[54:55], v[56:57], v[20:21]
	v_pk_fma_f32 v[50:51], v[50:51], v[56:57], v[16:17] neg_lo:[0,0,1] neg_hi:[0,0,1]
	v_mul_f32_e32 v16, v170, v53
	v_fract_f32_e32 v17, v16
	v_cos_f32_e32 v16, v17
	v_sin_f32_e32 v54, v17
	v_mul_f32_e32 v17, v171, v53
	v_fract_f32_e32 v53, v17
	v_cos_f32_e32 v17, v53
	v_sin_f32_e32 v55, v53
	v_pk_mul_f32 v[56:57], v[34:35], v[52:53] op_sel_hi:[1,0]
	s_nop 0
	v_pk_mul_f32 v[56:57], v[56:57], v[22:23]
	v_pk_mul_f32 v[22:23], v[38:39], v[52:53] op_sel_hi:[1,0]
	s_nop 0
	v_pk_mul_f32 v[18:19], v[22:23], v[18:19]
	s_nop 0
	v_pk_mul_f32 v[22:23], v[16:17], v[18:19]
	v_pk_mul_f32 v[18:19], v[54:55], v[18:19]
	v_pk_fma_f32 v[22:23], v[54:55], v[56:57], v[22:23]
	v_pk_fma_f32 v[52:53], v[16:17], v[56:57], v[18:19] neg_lo:[0,0,1] neg_hi:[0,0,1]
	v_lshlrev_b64 v[54:55], 11, v[48:49]
	s_cbranch_vccnz .LBB0_211
	v_lshl_add_u64 v[16:17], s[40:41], 0, v[54:55]
	s_lshl_b32 s72, s19, 1
	s_mov_b32 s73, s7
	v_lshl_add_u64 v[16:17], v[16:17], 0, s[72:73]
	v_lshl_add_u64 v[56:57], v[150:151], 1, v[16:17]
	v_pk_mul_f32 v[18:19], v[30:31], s[54:55] op_sel_hi:[1,0]
	v_pk_mul_f32 v[16:17], v[28:29], s[54:55] op_sel_hi:[1,0]
	v_pk_mul_f32 v[58:59], v[50:51], s[54:55] op_sel_hi:[1,0]
	v_pk_mul_f32 v[60:61], v[52:53], s[54:55] op_sel_hi:[1,0]
	v_cvt_pk_bf16_f32 v16, v16, v17
	v_cvt_pk_bf16_f32 v17, v18, v19
	v_cvt_pk_bf16_f32 v18, v58, v59
	s_mov_b64 s[72:73], 0
	v_cvt_pk_bf16_f32 v19, v60, v61
	global_store_dwordx4 v[56:57], v[16:19], off
	v_lshl_add_u64 v[56:57], v[56:57], 0, s[52:53]
	v_pk_mul_f32 v[58:59], v[20:21], s[54:55] op_sel_hi:[1,0]
	v_pk_mul_f32 v[18:19], v[26:27], s[54:55] op_sel_hi:[1,0]
	v_pk_mul_f32 v[16:17], v[24:25], s[54:55] op_sel_hi:[1,0]
	v_pk_mul_f32 v[60:61], v[22:23], s[54:55] op_sel_hi:[1,0]
	v_cvt_pk_bf16_f32 v16, v16, v17
	v_cvt_pk_bf16_f32 v17, v18, v19
	v_cvt_pk_bf16_f32 v18, v58, v59
	s_nop 0
	v_cvt_pk_bf16_f32 v19, v60, v61

; #define GAS __attribute__((address_space(1)))
; __device__ __forceinline__ v4u pack8(const f32x4 a, const f32x4 b) { v4u w; w.x = cvt_pk_bf16(a[0], a[1]); w.y = cvt_pk_bf16(a[2], a[3]); w.z = cvt_pk_bf16(b[0], b[1]); w.w = cvt_pk_bf16(b[2], b[3]); return w; }
; __device__ __forceinline__ float fexp(float x) { return __builtin_amdgcn_exp2f(x * 1.4426950408889634f); }
; __device__ __forceinline__ void cs_rev(float rev, float& c, float& s) { const float f = __builtin_amdgcn_fractf(rev); c = __builtin_amdgcn_cosf(f); s = __builtin_amdgcn_sinf(f); }
; #define EPI_LOOP_AM for (int ai = 0; ai < 2; ++ai) _Pragma("unroll") for (int m = 0; m < 4; ++m)
;     __device__ __forceinline__ void operator()(AccI& acci, const Unit& u, LAS unsigned char*, int wr, int wc, int fr, int fq) const {
;     ...
;             EPI_LOOP_AM {
;                 const int r = 128 * ai + 64 * wr + 16 * m + fr, tok = pm * 256 + r; const float pos = (float)tok; const float sxr = sx0[tok];
;                 f32x4 o1[2], o2[2];
; #pragma unroll
;                 for (int n = 0; n < 2; ++n)
; #pragma unroll
;                     for (int j = 0; j < 4; ++j) { float c, s; cs_rev(pos * inv[4 * n + j], c, s); const float x1 = ACCF(ai, 0, m, n, j), x2 = ACCF(ai, 1, m, n, j); o1[n][j] = x1 * c - x2 * s; o2[n][j] = x2 * c + x1 * s; }
;                 if (isq) {
;                     bf16* q = qs + (size_t)tok * RW + h * HD + c0; *(GAS v4u*)q = pack8(o1[0], o1[1]); *(GAS v4u*)(q + 128) = pack8(o2[0], o2[1]);
;                     const int il = r; const float wf = fexp(lgf * (float)(il + 1)), wb = fexp(lgb * (float)(255 - il));
;                     bf16* a = Acat + ((size_t)h * T + tok) * CAT + c0;
;                     *(GAS v4u*)(a + 256) = pack8(o1[0] * wf, o1[1] * wf); *(GAS v4u*)(a + 384) = pack8(o2[0] * wf, o2[1] * wf);
;                     *(GAS v4u*)(a + 512) = pack8(o1[0] * wb, o1[1] * wb); *(GAS v4u*)(a + 640) = pack8(o2[0] * wb, o2[1] * wb);
;                 } else {
;                     bf16* k = kk + (size_t)tok * RW + h * HD + c0; *(GAS v4u*)k = pack8(o1[0] * 0.0625f, o1[1] * 0.0625f); *(GAS v4u*)(k + 128) = pack8(o2[0] * 0.0625f, o2[1] * 0.0625f);
;                 }
.LBB0_213:
	global_store_dwordx4 v[56:57], v[16:19], off
	v_cvt_f32_i32_e32 v9, v9
	v_cvt_f32_i32_e32 v8, v8
	v_add_u32_e32 v16, 0xb0, v144
	v_ashrrev_i32_e32 v17, 31, v16
	v_lshl_add_u64 v[18:19], v[16:17], 2, s[34:35]
	v_mov_b32_e32 v20, v222
	v_cvt_f32_i32_e32 v21, v16
	v_cvt_f32_i32_e32 v11, v11
	v_cvt_f32_i32_e32 v10, v10
	v_cvt_f32_i32_e32 v1, v1
	v_mul_f32_e32 v22, v148, v21
	v_mul_f32_e32 v23, v165, v21
	v_mul_f32_e32 v24, v166, v21
	v_mul_f32_e32 v25, v167, v21
	v_mul_f32_e32 v26, v168, v21
	v_mul_f32_e32 v27, v169, v21
	v_mul_f32_e32 v28, v170, v21
	v_mul_f32_e32 v21, v171, v21
	v_cvt_f32_i32_e32 v0, v0
	v_cvt_f32_i32_e32 v3, v3
	v_cvt_f32_i32_e32 v2, v2
	v_fract_f32_e32 v29, v22
	v_fract_f32_e32 v30, v23
	v_fract_f32_e32 v31, v24
	v_fract_f32_e32 v48, v25
	v_fract_f32_e32 v49, v26
	v_fract_f32_e32 v50, v27
	v_fract_f32_e32 v51, v28
	v_fract_f32_e32 v21, v21
	v_cvt_f32_i32_e32 v13, v13
	v_cvt_f32_i32_e32 v12, v12
	v_cvt_f32_i32_e32 v15, v15
	v_cvt_f32_i32_e32 v14, v14
	v_cvt_f32_i32_e32 v5, v5
	v_cvt_f32_i32_e32 v4, v4
	v_cvt_f32_i32_e32 v7, v7
	v_cvt_f32_i32_e32 v6, v6
	v_cos_f32_e32 v22, v29
	v_sin_f32_e32 v24, v29
	v_cos_f32_e32 v23, v30
	v_sin_f32_e32 v25, v30
	v_cos_f32_e32 v26, v31
	v_sin_f32_e32 v28, v31
	v_cos_f32_e32 v27, v48
	v_sin_f32_e32 v29, v48
	v_cos_f32_e32 v30, v49
	v_sin_f32_e32 v48, v49
	v_cos_f32_e32 v31, v50
	v_sin_f32_e32 v49, v50
	v_cos_f32_e32 v50, v51
	v_sin_f32_e32 v52, v51
	v_cos_f32_e32 v51, v21
	v_sin_f32_e32 v53, v21
	v_lshlrev_b64 v[18:19], 11, v[16:17]
	s_and_b64 vcc, exec, s[4:5]
	s_mov_b64 s[4:5], -1
	v_pk_mul_f32 v[40:41], v[40:41], v[20:21] op_sel_hi:[1,0]
	v_pk_mul_f32 v[44:45], v[44:45], v[20:21] op_sel_hi:[1,0]
	v_pk_mul_f32 v[42:43], v[42:43], v[20:21] op_sel_hi:[1,0]
	v_pk_mul_f32 v[46:47], v[46:47], v[20:21] op_sel_hi:[1,0]
	v_pk_mul_f32 v[32:33], v[32:33], v[20:21] op_sel_hi:[1,0]
	v_pk_mul_f32 v[36:37], v[36:37], v[20:21] op_sel_hi:[1,0]
	v_pk_mul_f32 v[34:35], v[34:35], v[20:21] op_sel_hi:[1,0]
	v_pk_mul_f32 v[20:21], v[38:39], v[20:21] op_sel_hi:[1,0]
	v_pk_mul_f32 v[8:9], v[44:45], v[8:9]
	v_pk_mul_f32 v[10:11], v[46:47], v[10:11]
	v_pk_mul_f32 v[0:1], v[36:37], v[0:1]
	v_pk_mul_f32 v[2:3], v[20:21], v[2:3]
	v_pk_mul_f32 v[12:13], v[40:41], v[12:13]
	v_pk_mul_f32 v[14:15], v[42:43], v[14:15]
	v_pk_mul_f32 v[32:33], v[32:33], v[4:5]
	v_pk_mul_f32 v[34:35], v[34:35], v[6:7]
	v_pk_mul_f32 v[4:5], v[22:23], v[8:9]
	v_pk_mul_f32 v[6:7], v[24:25], v[8:9]
	v_pk_mul_f32 v[20:21], v[26:27], v[10:11]
	v_pk_mul_f32 v[10:11], v[28:29], v[10:11]
	v_pk_mul_f32 v[36:37], v[30:31], v[0:1]
	v_pk_mul_f32 v[38:39], v[48:49], v[0:1]
	v_pk_mul_f32 v[40:41], v[50:51], v[2:3]
	v_pk_mul_f32 v[42:43], v[52:53], v[2:3]
	v_pk_fma_f32 v[0:1], v[24:25], v[12:13], v[4:5]
	v_pk_fma_f32 v[8:9], v[22:23], v[12:13], v[6:7] neg_lo:[0,0,1] neg_hi:[0,0,1]
	v_pk_fma_f32 v[2:3], v[28:29], v[14:15], v[20:21]
	v_pk_fma_f32 v[12:13], v[26:27], v[14:15], v[10:11] neg_lo:[0,0,1] neg_hi:[0,0,1]
	v_pk_fma_f32 v[4:5], v[48:49], v[32:33], v[36:37]
	v_pk_fma_f32 v[10:11], v[30:31], v[32:33], v[38:39] neg_lo:[0,0,1] neg_hi:[0,0,1]
	v_pk_fma_f32 v[6:7], v[52:53], v[34:35], v[40:41]
	v_pk_fma_f32 v[14:15], v[50:51], v[34:35], v[42:43] neg_lo:[0,0,1] neg_hi:[0,0,1]
	s_cbranch_vccnz .LBB0_215
	v_lshl_add_u64 v[20:21], s[40:41], 0, v[18:19]
	s_lshl_b32 s4, s19, 1
	s_mov_b32 s5, s7
	v_lshl_add_u64 v[20:21], v[20:21], 0, s[4:5]
	v_lshl_add_u64 v[24:25], v[150:151], 1, v[20:21]
	v_pk_mul_f32 v[22:23], v[12:13], s[54:55] op_sel_hi:[1,0]
	v_pk_mul_f32 v[20:21], v[8:9], s[54:55] op_sel_hi:[1,0]
	v_pk_mul_f32 v[26:27], v[10:11], s[54:55] op_sel_hi:[1,0]
	v_pk_mul_f32 v[28:29], v[14:15], s[54:55] op_sel_hi:[1,0]
	v_cvt_pk_bf16_f32 v20, v20, v21
	v_cvt_pk_bf16_f32 v21, v22, v23
	v_cvt_pk_bf16_f32 v22, v26, v27
	v_lshl_add_u64 v[152:153], v[24:25], 0, s[52:53]
	v_cvt_pk_bf16_f32 v23, v28, v29
	s_mov_b64 s[4:5], 0
	global_store_dwordx4 v[24:25], v[20:23], off
	v_pk_mul_f32 v[26:27], v[4:5], s[54:55] op_sel_hi:[1,0]
	v_pk_mul_f32 v[28:29], v[6:7], s[54:55] op_sel_hi:[1,0]
	v_pk_mul_f32 v[20:21], v[2:3], s[54:55] op_sel_hi:[1,0]
	v_pk_mul_f32 v[22:23], v[0:1], s[54:55] op_sel_hi:[1,0]
	s_nop 0
	v_cvt_pk_bf16_f32 v144, v22, v23
	v_cvt_pk_bf16_f32 v145, v20, v21
	v_cvt_pk_bf16_f32 v146, v26, v27
	v_cvt_pk_bf16_f32 v147, v28, v29
